# GU L0+L1 K-loops: each half keeps only half of the per-interval barriers (older half computes first), stagger/align barriers removed
# baseline (speedup 1.0000x reference)
;     ...
;     for (int i = 0; i < 2; ++i) { stage_rc(tid * 16 + i * 8192, sR[i], sC[i]); const int Rb = Epi::PERM ? ((sR[i] & ~31) + perm32(sR[i] & 31)) : sR[i];
;         voffB[i] = (TILED & 2) ? (unsigned)(Rb * BK + sC[i]) * 2u : (unsigned)(Rb * K + sC[i]) * 2u; }
;     constexpr size_t kstepA = (TILED & 1) ? (size_t)HALF * BK * 2 : (size_t)(BK * 2), kstepB = (TILED & 2) ? (size_t)HALF * BK * 2 : (size_t)(BK * 2);
;     const size_t hstep = (size_t)HALF * K * 2;
;     const size_t tstep = 2 * hstep;
;     const unsigned ldsw = (unsigned)wid * 1024u;
;     const int aoff = lds_byte(wr * 64 + fr, fq * 8), boff = lds_byte(wc * 32 + fr, fq * 8);
;     ...
;     Unit cur, nxt; int ui = 0;
;     if (!S.next(0, cur)) return;
;     if constexpr (GATHER) {
;         for (int k = tid >> 8;; k += 2) { Unit u; if (!S.next(k, u)) break; idxl[k * 256 + (tid & 255)] = g.ridx[(size_t)u.z * g.ridxStrideZ + u.pm * BM + (tid & 255)]; }
;         __syncthreads();
; #pragma unroll
;         for (int hh = 0; hh < 2; ++hh)
; #pragma unroll
;             for (int i = 0; i < 2; ++i) voffA[hh][i] = (unsigned)idxl[hh * HALF + sR[i]] * (unsigned)(K * 2) + (unsigned)sC[i] * 2u;
;     } else {
; #pragma unroll
;         for (int hh = 0; hh < 2; ++hh)
; #pragma unroll
;             for (int i = 0; i < 2; ++i) voffA[hh][i] = (TILED & 1) ? (unsigned)hh * (unsigned)(HALF * K * 2) + (unsigned)(sR[i] * BK + sC[i]) * 2u : (unsigned)((hh * HALF + sR[i]) * K + sC[i]) * 2u;
;     }
; #pragma unroll
;     for (int hh = 0; hh < 2; ++hh)
; #pragma unroll
;         for (int i = 0; i < 2; ++i) voffN[hh][i] = voffA[hh][i];
;     f32x4 acc[2][2][4][2];
; #pragma unroll
;     for (int a = 0; a < 2; ++a)
; #pragma unroll
;         for (int b = 0; b < 2; ++b)
; #pragma unroll
;             for (int m = 0; m < 4; ++m)
; #pragma unroll
;                 for (int n = 0; n < 2; ++n) acc[a][b][m][n] = (f32x4){0.f, 0.f, 0.f, 0.f};
;     bf16x8 At[4][2], B0[2][2], B1[2][2];
;     auto k0t = [&](const Unit& u) -> size_t { return (SPLITK && u.kq >= 0) ? (size_t)(12 * u.kq - (u.kq == 3 ? 2 : 0)) : (size_t)0; };
;     const char* cA = (const char*)(g.A + (size_t)cur.z * g.aStrideZ) + (GATHER ? (size_t)0 : (size_t)cur.pm * tstep) + k0t(cur) * kstepA;
;     const char* cB = (const char*)(g.Bt + (size_t)cur.z * g.bStrideZ) + (size_t)cur.pn * tstep + k0t(cur) * kstepB;
.LBB0_995:
	s_or_b64 exec, exec, s[0:1]
	v_ashrrev_i32_e32 v4, 31, v1
	v_lshrrev_b32_e32 v4, 22, v4
	v_add_u32_e32 v4, v1, v4
	v_add_u32_e32 v2, 0x2000, v1
	v_and_b32_e32 v4, 0xfc00, v4
	v_sub_u32_e32 v1, v1, v4
	v_ashrrev_i32_e32 v4, 31, v2
	v_lshrrev_b32_e32 v4, 22, v4
	v_add_u32_e32 v4, v2, v4
	v_ashrrev_i32_e32 v5, 10, v4
	v_and_b32_e32 v4, 0xfc00, v4
	v_ashrrev_i32_e32 v3, 31, v6
	v_sub_u32_e32 v2, v2, v4
	s_mov_b32 s0, 0x5040100
	v_lshrrev_b32_e32 v3, 26, v3
	v_perm_b32 v1, v2, v1, s0
	v_add_u32_e32 v3, v6, v3
	v_pk_ashrrev_i16 v1, 4, v1 op_sel_hi:[0,1]
	v_mov_b32_e32 v4, 3
	v_ashrrev_i32_e32 v3, 6, v3
	v_ashrrev_i32_sdwa v4, v4, sext(v1) dst_sel:DWORD dst_unused:UNUSED_PAD src0_sel:DWORD src1_sel:WORD_0
	v_lshl_add_u32 v199, v3, 3, v4
	v_lshlrev_b32_e32 v3, 1, v199
	v_lshrrev_b32_e32 v7, 2, v199
	v_and_b32_e32 v8, 3, v4
	s_mov_b32 s0, 0x1ffffe0
	v_ashrrev_i32_e32 v2, 19, v1
	v_and_b32_e32 v3, 24, v3
	v_and_b32_e32 v7, 4, v7
	v_and_or_b32 v8, v199, s0, v8
	v_or3_b32 v3, v8, v7, v3
	v_xor_b32_sdwa v7, v2, sext(v1) dst_sel:DWORD dst_unused:UNUSED_PAD src0_sel:DWORD src1_sel:WORD_1
	v_xor_b32_sdwa v1, v4, sext(v1) dst_sel:DWORD dst_unused:UNUSED_PAD src0_sel:DWORD src1_sel:WORD_0
	v_lshlrev_b32_e32 v4, 4, v7
	v_lshlrev_b32_e32 v7, 4, v1
	v_and_b32_e32 v200, 0x70, v7
	v_lshl_add_u32 v201, v5, 3, v2
	v_and_b32_e32 v1, 0x70, v4
	v_lshl_or_b32 v202, v3, 7, v200
	v_lshlrev_b32_e32 v3, 1, v201
	v_lshrrev_b32_e32 v4, 2, v201
	v_and_b32_e32 v2, 3, v2
	v_and_b32_e32 v3, 24, v3
	v_and_b32_e32 v4, 4, v4
	v_and_or_b32 v2, v201, s0, v2
	v_or3_b32 v2, v2, v4, v3
	v_lshl_or_b32 v204, v2, 7, v1
	s_ashr_i32 s0, s4, 6
	v_lshlrev_b32_e32 v2, 2, v199
	s_add_i32 s2, 0, 0x20000
	v_lshlrev_b32_e32 v4, 2, v201
	s_ashr_i32 s1, s4, 8
	s_lshl_b32 s5, s0, 10
	v_add_u32_e32 v3, s2, v2
	v_add_u32_e32 v5, s2, v4
	s_add_i32 s2, 0, 0x20200
	s_mul_i32 s3, s62, 0xb00000
	v_readlane_b32 s6, v250, 6
	v_add_u32_e32 v2, s2, v2
	v_add_u32_e32 v4, s2, v4
	s_mul_hi_i32 s2, s62, 0xb00000
	v_readlane_b32 s7, v250, 7
	s_add_u32 s6, s6, s3
	s_addc_u32 s7, s7, s2
	s_ashr_i32 s23, s22, 31
	s_lshl_b64 s[2:3], s[22:23], 19
	s_add_u32 s6, s6, s2
	s_addc_u32 s7, s7, s3
	s_add_i32 s23, s5, 0
	s_waitcnt lgkmcnt(0)
	s_barrier
	ds_read_b32 v3, v3
	ds_read_b32 v5, v5
	s_add_i32 s37, s23, 0x10000
	s_add_i32 s38, s23, 0x12000
	s_mov_b32 m0, s37
	s_add_u32 s2, s6, 0x40000
	ds_read_b32 v2, v2
	ds_read_b32 v4, v4
	global_load_lds_dwordx4 v202, s[6:7]
	s_mov_b32 m0, s38
	s_addc_u32 s3, s7, 0
	s_add_i32 s39, s23, 0x14000
	global_load_lds_dwordx4 v204, s[6:7]
	s_mov_b32 m0, s39
	s_add_i32 s40, s23, 0x16000
	s_waitcnt lgkmcnt(0)
	v_lshlrev_b32_e32 v3, 11, v3
	global_load_lds_dwordx4 v202, s[2:3]
	s_mov_b32 m0, s40
	v_lshlrev_b32_e32 v5, 11, v5
	v_or_b32_e32 v218, v3, v200
	global_load_lds_dwordx4 v204, s[2:3]
	s_mov_b32 m0, s23
	s_add_i32 s41, s23, 0x2000
	v_or_b32_e32 v219, v5, v1
	global_load_lds_dwordx4 v218, s[82:83]
	s_mov_b32 m0, s41
	s_add_i32 s42, s23, 0x4000
	v_lshl_or_b32 v214, v2, 11, v200
	global_load_lds_dwordx4 v219, s[82:83]
	s_mov_b32 m0, s42
	s_add_i32 s43, s23, 0x6000
	v_lshl_or_b32 v216, v4, 11, v1
	global_load_lds_dwordx4 v214, s[82:83]
	s_mov_b32 m0, s43
	v_mov_b32_e32 v3, 0
	global_load_lds_dwordx4 v216, s[82:83]
	s_cmp_eq_u32 s1, 1
	s_mov_b32 s44, 0
	v_mov_b32_e32 v203, v3
	v_mov_b32_e32 v205, v3
	v_mov_b32_e32 v2, v218
	v_mov_b32_e32 v4, v219
	s_cselect_b64 s[2:3], -1, 0
	s_cmp_lg_u32 s1, 1
	v_mov_b32_e32 v5, v3
	s_cbranch_scc1 .LBB0_997
.LBB0_997:
	s_lshl_b32 s45, s1, 6
	s_lshl_b32 s1, s0, 5
	s_and_b32 s46, s1, 0x60
	s_add_u32 s8, s6, 0x4000
	s_addc_u32 s9, s7, 0
	s_add_i32 s47, s23, 0x18000
	s_add_i32 s48, s23, 0x1a000
	v_lshl_add_u64 v[8:9], s[8:9], 0, v[202:203]
	s_mov_b32 m0, s47
	s_add_u32 s12, s90, 0x4213680
	s_waitcnt vmcnt(2)
	s_barrier
	global_load_lds_dwordx4 v[8:9], off
	v_lshl_add_u64 v[8:9], s[8:9], 0, v[204:205]
	s_mov_b32 m0, s48
	s_addc_u32 s13, s91, 0
	s_add_i32 s49, s23, 0x8000
	s_add_i32 s50, s23, 0xa000
	global_load_lds_dwordx4 v[8:9], off
	v_lshl_add_u64 v[8:9], s[12:13], 0, v[2:3]
	s_mov_b32 m0, s49
	s_add_u32 s8, s6, 0x44000
	global_load_lds_dwordx4 v[8:9], off
	v_lshl_add_u64 v[4:5], s[12:13], 0, v[4:5]
	s_mov_b32 m0, s50
	s_addc_u32 s9, s7, 0
	s_add_i32 s51, s23, 0x1c000
	global_load_lds_dwordx4 v[4:5], off
	v_lshl_add_u64 v[4:5], s[8:9], 0, v[202:203]
	s_mov_b32 m0, s51
	s_add_i32 s52, s23, 0x1e000
	global_load_lds_dwordx4 v[4:5], off
	v_lshl_add_u64 v[4:5], s[8:9], 0, v[204:205]
	s_mov_b32 m0, s52
	v_lshrrev_b32_e32 v2, 4, v6
	global_load_lds_dwordx4 v[4:5], off
	v_and_b32_e32 v4, 15, v6
	v_bfe_u32 v5, v6, 4, 2
	v_and_b32_e32 v6, 7, v6
	s_cmpk_lt_u32 s4, 0x100
	v_bitop3_b32 v2, v2, v6, 3 bitop3:0x6c
	s_cselect_b64 s[14:15], -1, 0
	s_lshl_b32 s0, s0, 6
	v_lshlrev_b32_e32 v8, 4, v2
	v_or_b32_e32 v2, s46, v4
	s_and_b32 s0, s0, 64
	v_lshlrev_b32_e32 v10, 7, v2
	v_lshl_or_b32 v2, v5, 4, s0
	v_readlane_b32 s0, v250, 32
	v_or_b32_e32 v7, s45, v4
	v_and_or_b32 v4, s45, 64, v4
	v_readlane_b32 s1, v250, 33
	v_lshlrev_b32_e32 v7, 7, v7
	s_waitcnt vmcnt(6)
	v_or_b32_e32 v9, v7, v8
	v_lshl_add_u64 v[206:207], s[0:1], 0, v[2:3]
	v_lshlrev_b32_e32 v2, 6, v4
	v_or_b32_e32 v4, 0x800, v2
	v_or_b32_e32 v6, 0xc00, v2
	v_bitop3_b32 v5, v7, 64, v8 bitop3:0x36
	s_lshl_b32 s0, s94, 1
	v_or_b32_e32 v226, v10, v8
	v_bitop3_b32 v227, v10, 64, v8 bitop3:0x36
	s_and_b32 s53, s0, 14
	s_add_i32 s54, 0, 0x10000
	s_add_i32 s55, 0, 0x10800
	s_add_i32 s56, 0, 0x14000
	s_add_i32 s57, 0, 0x14800
	s_add_i32 s58, 0, 0x18800
	s_add_i32 s59, 0, 0x1c800
	s_mov_b64 s[16:17], 0x80
	v_lshlrev_b32_e32 v208, 1, v2
	v_lshlrev_b32_e32 v210, 1, v4
	v_lshlrev_b32_e32 v212, 1, v6
	v_add_u32_e32 v228, 0, v9
	v_add_u32_e32 v229, 0, v5
	v_mov_b32_e32 v230, 0xc60000
	s_barrier
	s_branch .LBB0_1000

; #define PG8_WAIT_V(n) asm volatile("s_waitcnt vmcnt(" #n ")" ::: "memory")
; #define PG8_WAIT_L(n) asm volatile("s_waitcnt lgkmcnt(" #n ")" ::: "memory")
;     ...
;         for (int t = 0; t < nt; t += 2) {
;             const bool last = (t == nt - 2);
;             const char* a1 = cA + (size_t)(t + 1) * kstepA;
;             const char* a2 = last ? nA : cA + (size_t)(t + 2) * kstepA; const char* b2 = last ? nB : cB + (size_t)(t + 2) * kstepB;
;             const char* a3 = a2 + kstepA; const char* b3 = b2 + kstepB;
;             unsigned vs[2][2];
;             if constexpr (GATHER) {
;                 if (last && has_next) {
; #pragma unroll
;                     for (int hh = 0; hh < 2; ++hh)
; #pragma unroll
;                         for (int i = 0; i < 2; ++i) voffN[hh][i] = (unsigned)idxl[(ui + 1) * 256 + hh * HALF + sR[i]] * (unsigned)(K * 2) + (unsigned)sC[i] * 2u;
;                 }
; #pragma unroll
;                 for (int hh = 0; hh < 2; ++hh)
; #pragma unroll
;                     for (int i = 0; i < 2; ++i) vs[hh][i] = last ? voffN[hh][i] : voffA[hh][i];
;             } else {
; #pragma unroll
;                 for (int hh = 0; hh < 2; ++hh)
; #pragma unroll
;                     for (int i = 0; i < 2; ++i) vs[hh][i] = voffA[hh][i];
;             }
;             PG8_LDB(B0, 0, 0); PG8_LDB(B1, 0, 1); PG8_SCHED; PG8_LDA(At, 0, 0); PG8_STAGE(PG8_SA(1, 1), a1, voffA[1]);
;             PG8_WAIT_V(8); PG8_WAIT_L(0); PG8_BAR; if (do0) { PG8_MMA(0, 0, At, B0); PG8_MMA(0, 1, At, B1); } PG8_BAR; PG8_SCHED;
;             PG8_LDA(At, 0, 1); PG8_STAGE(PG8_SB(0, 0), b2, voffB); PG8_STAGE(PG8_SB(0, 1), b2 + hstep, voffB); PG8_STAGE(PG8_SA(0, 0), a2, vs[0]);
;             PG8_WAIT_V(8); PG8_WAIT_L(0); PG8_BAR; if (do1) { PG8_MMA(1, 0, At, B0); PG8_MMA(1, 1, At, B1); } PG8_BAR; PG8_SCHED;
;             PG8_LDB(B0, 1, 0); PG8_LDB(B1, 1, 1); PG8_SCHED; PG8_LDA(At, 1, 0); PG8_STAGE(PG8_SA(0, 1), a2, vs[1]);
;             PG8_WAIT_V(8); PG8_WAIT_L(0); PG8_BAR; if (do0) { PG8_MMA(0, 0, At, B0); PG8_MMA(0, 1, At, B1); } PG8_BAR; PG8_SCHED;
;             PG8_LDA(At, 1, 1); PG8_STAGE(PG8_SB(1, 0), b3, voffB); PG8_STAGE(PG8_SB(1, 1), b3 + hstep, voffB); PG8_STAGE(PG8_SA(1, 0), a3, vs[0]);
;             PG8_WAIT_V(8); PG8_WAIT_L(0); PG8_BAR; if (do1) { PG8_MMA(1, 0, At, B0); PG8_MMA(1, 1, At, B1); } PG8_BAR; PG8_SCHED;
;         }
.LBB0_1005:
	s_bitcmp1_b32 s2, 0
	s_cbranch_scc0 .Lsb_guL0_0
	s_barrier
.Lsb_guL0_0:
	s_add_i32 s65, s65, 2
	s_add_u32 s19, s19, 0x8000
	s_addc_u32 s64, s64, 0
	s_add_u32 s28, s28, 0x100
	s_addc_u32 s29, s29, 0
	s_cmp_gt_u32 s65, 13
	s_cbranch_scc1 .LBB0_1016

; #define PG8_STAGE(bufoff, gbase, voff) do { _Pragma("unroll") for (int _i = 0; _i < 2; ++_i) \
;         __builtin_amdgcn_global_load_lds((const unsigned*)((const char*)(gbase) + (voff)[_i]), (LAS unsigned*)(lds + (bufoff) + ldsw + _i * 8192), 16, 0, 0); } while (0)
; #define PG8_LDA(dst, b, h) do { _Pragma("unroll") for (int m = 0; m < 4; ++m) _Pragma("unroll") for (int k = 0; k < 2; ++k) dst[m][k] = *(const LAS bf16x8*)(lds + PG8_SA(b, h) + ((aoff ^ (k * 64)) + m * 2048)); } while (0)
; #define PG8_LDB(dst, b, h) do { _Pragma("unroll") for (int n = 0; n < 2; ++n) _Pragma("unroll") for (int k = 0; k < 2; ++k) dst[n][k] = *(const LAS bf16x8*)(lds + PG8_SB(b, h) + ((boff ^ (k * 64)) + n * 2048)); } while (0)
; #define PG8_BAR __builtin_amdgcn_s_barrier()
;     ...
;             const bool last = (t == nt - 2);
;             const char* a1 = cA + (size_t)(t + 1) * kstepA;
;             const char* a2 = last ? nA : cA + (size_t)(t + 2) * kstepA; const char* b2 = last ? nB : cB + (size_t)(t + 2) * kstepB;
;             const char* a3 = a2 + kstepA; const char* b3 = b2 + kstepB;
;             unsigned vs[2][2];
;             if constexpr (GATHER) {
;                 if (last && has_next) {
; #pragma unroll
;                     for (int hh = 0; hh < 2; ++hh)
; #pragma unroll
;                         for (int i = 0; i < 2; ++i) voffN[hh][i] = (unsigned)idxl[(ui + 1) * 256 + hh * HALF + sR[i]] * (unsigned)(K * 2) + (unsigned)sC[i] * 2u;
;                 }
; #pragma unroll
;                 for (int hh = 0; hh < 2; ++hh)
; #pragma unroll
;                     for (int i = 0; i < 2; ++i) vs[hh][i] = last ? voffN[hh][i] : voffA[hh][i];
;             } else {
; #pragma unroll
;                 for (int hh = 0; hh < 2; ++hh)
; #pragma unroll
;                     for (int i = 0; i < 2; ++i) vs[hh][i] = voffA[hh][i];
;             }
;             PG8_LDB(B0, 0, 0); PG8_LDB(B1, 0, 1); PG8_SCHED; PG8_LDA(At, 0, 0); PG8_STAGE(PG8_SA(1, 1), a1, voffA[1]);
;             PG8_WAIT_V(8); PG8_WAIT_L(0); PG8_BAR; if (do0) { PG8_MMA(0, 0, At, B0); PG8_MMA(0, 1, At, B1); } PG8_BAR; PG8_SCHED;
;             PG8_LDA(At, 0, 1); PG8_STAGE(PG8_SB(0, 0), b2, voffB); PG8_STAGE(PG8_SB(0, 1), b2 + hstep, voffB); PG8_STAGE(PG8_SA(0, 0), a2, vs[0]);
;             PG8_WAIT_V(8); PG8_WAIT_L(0); PG8_BAR; if (do1) { PG8_MMA(1, 0, At, B0); PG8_MMA(1, 1, At, B1); } PG8_BAR; PG8_SCHED;
.LBB0_1008:
	v_add_u32_e32 v2, s54, v226
	v_add_u32_e32 v134, s54, v227
	ds_read_b128 v[150:153], v2
	ds_read_b128 v[154:157], v134
	v_add_u32_e32 v2, s55, v226
	v_add_u32_e32 v134, s55, v227
	ds_read_b128 v[158:161], v2
	ds_read_b128 v[162:165], v134
	v_add_u32_e32 v2, s56, v226
	v_add_u32_e32 v138, s56, v227
	ds_read_b128 v[134:137], v2
	ds_read_b128 v[138:141], v138
	v_add_u32_e32 v2, s57, v226
	v_add_u32_e32 v146, s57, v227
	ds_read_b128 v[142:145], v2
	ds_read_b128 v[146:149], v146
	v_lshl_add_u64 v[224:225], v[222:223], 0, s[28:29]
	s_add_i32 m0, s23, 0xc000
	s_waitcnt lgkmcnt(0)
	ds_read_b128 v[190:193], v228
	ds_read_b128 v[178:181], v228 offset:2048
	ds_read_b128 v[194:197], v229
	ds_read_b128 v[182:185], v229 offset:2048
	ds_read_b128 v[174:177], v228 offset:4096
	ds_read_b128 v[166:169], v228 offset:6144
	ds_read_b128 v[186:189], v229 offset:4096
	ds_read_b128 v[170:173], v229 offset:6144
	global_load_lds_dwordx4 v[224:225], off
	v_lshl_add_u64 v[224:225], v[220:221], 0, s[28:29]
	s_add_i32 m0, s23, 0xe000
	v_cndmask_b32_e64 v2, 0, 1, s[26:27]
	global_load_lds_dwordx4 v[224:225], off
	s_waitcnt vmcnt(8)
	s_waitcnt lgkmcnt(0)
	v_cmp_ne_u32_e64 s[8:9], 1, v2
	s_andn2_b64 vcc, exec, s[26:27]
	s_bitcmp0_b32 s2, 0
	s_cbranch_scc0 .Lsb_guL0_1
	s_barrier
.Lsb_guL0_1:
	s_cbranch_vccnz .LBB0_1010
	s_setprio 1
	s_waitcnt lgkmcnt(0)
	v_mfma_f32_16x16x32_bf16 v[130:133], v[150:153], v[190:193], v[130:133]
	v_mfma_f32_16x16x32_bf16 v[126:129], v[158:161], v[190:193], v[126:129]
	v_mfma_f32_16x16x32_bf16 v[114:117], v[150:153], v[178:181], v[114:117]
	v_mfma_f32_16x16x32_bf16 v[110:113], v[158:161], v[178:181], v[110:113]
	v_mfma_f32_16x16x32_bf16 v[98:101], v[150:153], v[174:177], v[98:101]
	v_mfma_f32_16x16x32_bf16 v[94:97], v[158:161], v[174:177], v[94:97]
	v_mfma_f32_16x16x32_bf16 v[82:85], v[150:153], v[166:169], v[82:85]
	v_mfma_f32_16x16x32_bf16 v[78:81], v[158:161], v[166:169], v[78:81]
	v_mfma_f32_16x16x32_bf16 v[130:133], v[154:157], v[194:197], v[130:133]
	v_mfma_f32_16x16x32_bf16 v[126:129], v[162:165], v[194:197], v[126:129]
	v_mfma_f32_16x16x32_bf16 v[114:117], v[154:157], v[182:185], v[114:117]
	v_mfma_f32_16x16x32_bf16 v[110:113], v[162:165], v[182:185], v[110:113]
	v_mfma_f32_16x16x32_bf16 v[98:101], v[154:157], v[186:189], v[98:101]
	v_mfma_f32_16x16x32_bf16 v[94:97], v[162:165], v[186:189], v[94:97]
	v_mfma_f32_16x16x32_bf16 v[82:85], v[154:157], v[170:173], v[82:85]
	v_mfma_f32_16x16x32_bf16 v[78:81], v[162:165], v[170:173], v[78:81]
	s_setprio 0
	s_setprio 1
	v_mfma_f32_16x16x32_bf16 v[122:125], v[134:137], v[190:193], v[122:125]
	v_mfma_f32_16x16x32_bf16 v[118:121], v[142:145], v[190:193], v[118:121]
	v_mfma_f32_16x16x32_bf16 v[106:109], v[134:137], v[178:181], v[106:109]
	v_mfma_f32_16x16x32_bf16 v[102:105], v[142:145], v[178:181], v[102:105]
	v_mfma_f32_16x16x32_bf16 v[90:93], v[134:137], v[174:177], v[90:93]
	v_mfma_f32_16x16x32_bf16 v[86:89], v[142:145], v[174:177], v[86:89]
	v_mfma_f32_16x16x32_bf16 v[74:77], v[134:137], v[166:169], v[74:77]
	v_mfma_f32_16x16x32_bf16 v[70:73], v[142:145], v[166:169], v[70:73]
	v_mfma_f32_16x16x32_bf16 v[122:125], v[138:141], v[194:197], v[122:125]
	v_mfma_f32_16x16x32_bf16 v[118:121], v[146:149], v[194:197], v[118:121]
	v_mfma_f32_16x16x32_bf16 v[106:109], v[138:141], v[182:185], v[106:109]
	v_mfma_f32_16x16x32_bf16 v[102:105], v[146:149], v[182:185], v[102:105]
	v_mfma_f32_16x16x32_bf16 v[90:93], v[138:141], v[186:189], v[90:93]
	v_mfma_f32_16x16x32_bf16 v[86:89], v[146:149], v[186:189], v[86:89]
	v_mfma_f32_16x16x32_bf16 v[74:77], v[138:141], v[170:173], v[74:77]
	v_mfma_f32_16x16x32_bf16 v[70:73], v[146:149], v[170:173], v[70:73]
	s_setprio 0
.LBB0_1010:
	s_add_u32 s10, s90, s28
	s_addc_u32 s11, s91, s29
	s_add_u32 s30, s10, 0x4213700
	s_addc_u32 s31, s11, 0
	s_and_b64 s[10:11], s[6:7], exec
	v_cndmask_b32_e64 v2, v218, v4, s[6:7]
	v_cndmask_b32_e64 v224, v219, v5, s[6:7]
	s_cselect_b32 s35, s83, s31
	s_cselect_b32 s34, s82, s30
	s_cselect_b32 s31, s21, s64
	s_cselect_b32 s30, s20, s19
	s_bitcmp1_b32 s2, 0
	s_cbranch_scc0 .Lsb_guL0_2
	s_barrier
; #define PG8_STAGE(bufoff, gbase, voff) do { _Pragma("unroll") for (int _i = 0; _i < 2; ++_i) \
;         __builtin_amdgcn_global_load_lds((const unsigned*)((const char*)(gbase) + (voff)[_i]), (LAS unsigned*)(lds + (bufoff) + ldsw + _i * 8192), 16, 0, 0); } while (0)
; #define PG8_LDA(dst, b, h) do { _Pragma("unroll") for (int m = 0; m < 4; ++m) _Pragma("unroll") for (int k = 0; k < 2; ++k) dst[m][k] = *(const LAS bf16x8*)(lds + PG8_SA(b, h) + ((aoff ^ (k * 64)) + m * 2048)); } while (0)
; #define PG8_LDB(dst, b, h) do { _Pragma("unroll") for (int n = 0; n < 2; ++n) _Pragma("unroll") for (int k = 0; k < 2; ++k) dst[n][k] = *(const LAS bf16x8*)(lds + PG8_SB(b, h) + ((boff ^ (k * 64)) + n * 2048)); } while (0)
; #define PG8_MMA(ai, bj, At, Bt) do { __builtin_amdgcn_s_setprio(1); _Pragma("unroll") for (int m = 0; m < 4; ++m) _Pragma("unroll") for (int n = 0; n < 2; ++n) _Pragma("unroll") for (int k = 0; k < 2; ++k) \
;         acc[ai][bj][m][n] = __builtin_amdgcn_mfma_f32_16x16x32_bf16(Bt[n][k], At[m][k], acc[ai][bj][m][n], 0, 0, 0); __builtin_amdgcn_s_setprio(0); } while (0)
; #define PG8_WAIT_V(n) asm volatile("s_waitcnt vmcnt(" #n ")" ::: "memory")
; #define PG8_WAIT_L(n) asm volatile("s_waitcnt lgkmcnt(" #n ")" ::: "memory")
; #define PG8_BAR __builtin_amdgcn_s_barrier()
; #define PG8_SCHED __builtin_amdgcn_sched_barrier(0)
;     ...
;             PG8_LDA(At, 0, 1); PG8_STAGE(PG8_SB(0, 0), b2, voffB); PG8_STAGE(PG8_SB(0, 1), b2 + hstep, voffB); PG8_STAGE(PG8_SA(0, 0), a2, vs[0]);
;             PG8_WAIT_V(8); PG8_WAIT_L(0); PG8_BAR; if (do1) { PG8_MMA(1, 0, At, B0); PG8_MMA(1, 1, At, B1); } PG8_BAR; PG8_SCHED;
;             PG8_LDB(B0, 1, 0); PG8_LDB(B1, 1, 1); PG8_SCHED; PG8_LDA(At, 1, 0); PG8_STAGE(PG8_SA(0, 1), a2, vs[1]);
;             PG8_WAIT_V(8); PG8_WAIT_L(0); PG8_BAR; if (do0) { PG8_MMA(0, 0, At, B0); PG8_MMA(0, 1, At, B1); } PG8_BAR; PG8_SCHED;
.Lsb_guL0_2:
	s_mov_b32 m0, s37
	v_lshl_add_u64 v[232:233], s[30:31], 0, v[202:203]
	s_add_u32 s10, s30, 0x40000
	s_waitcnt lgkmcnt(0)
	ds_read_b128 v[190:193], v228 offset:16384
	ds_read_b128 v[178:181], v228 offset:18432
	ds_read_b128 v[194:197], v229 offset:16384
	ds_read_b128 v[182:185], v229 offset:18432
	ds_read_b128 v[174:177], v228 offset:20480
	ds_read_b128 v[166:169], v228 offset:22528
	ds_read_b128 v[186:189], v229 offset:20480
	ds_read_b128 v[170:173], v229 offset:22528
	global_load_lds_dwordx4 v[232:233], off
	v_lshl_add_u64 v[232:233], s[30:31], 0, v[204:205]
	s_mov_b32 m0, s38
	s_addc_u32 s11, s31, 0
	global_load_lds_dwordx4 v[232:233], off
	v_lshl_add_u64 v[232:233], s[10:11], 0, v[202:203]
	s_mov_b32 m0, s39
	v_cndmask_b32_e64 v213, 0, 1, s[24:25]
	global_load_lds_dwordx4 v[232:233], off
	v_lshl_add_u64 v[232:233], s[10:11], 0, v[204:205]
	s_mov_b32 m0, s40
	v_cmp_ne_u32_e64 s[10:11], 1, v213
	global_load_lds_dwordx4 v[232:233], off
	s_mov_b32 m0, s23
	s_andn2_b64 vcc, exec, s[24:25]
	global_load_lds_dwordx4 v2, s[34:35]
	s_mov_b32 m0, s41
	s_nop 0
	global_load_lds_dwordx4 v224, s[34:35]
	s_waitcnt vmcnt(8)
	s_waitcnt lgkmcnt(0)
	s_bitcmp0_b32 s2, 0
	s_cbranch_scc0 .Lsb_guL0_3
	s_barrier
.Lsb_guL0_3:
	s_cbranch_vccnz .LBB0_1012
	s_setprio 1
	s_waitcnt lgkmcnt(0)
	v_mfma_f32_16x16x32_bf16 v[66:69], v[150:153], v[190:193], v[66:69]
	v_mfma_f32_16x16x32_bf16 v[62:65], v[158:161], v[190:193], v[62:65]
	v_mfma_f32_16x16x32_bf16 v[50:53], v[150:153], v[178:181], v[50:53]
	v_mfma_f32_16x16x32_bf16 v[46:49], v[158:161], v[178:181], v[46:49]
	v_mfma_f32_16x16x32_bf16 v[34:37], v[150:153], v[174:177], v[34:37]
	v_mfma_f32_16x16x32_bf16 v[30:33], v[158:161], v[174:177], v[30:33]
	v_mfma_f32_16x16x32_bf16 v[18:21], v[150:153], v[166:169], v[18:21]
	v_mfma_f32_16x16x32_bf16 v[14:17], v[158:161], v[166:169], v[14:17]
	v_mfma_f32_16x16x32_bf16 v[66:69], v[154:157], v[194:197], v[66:69]
	v_mfma_f32_16x16x32_bf16 v[62:65], v[162:165], v[194:197], v[62:65]
	v_mfma_f32_16x16x32_bf16 v[50:53], v[154:157], v[182:185], v[50:53]
	v_mfma_f32_16x16x32_bf16 v[46:49], v[162:165], v[182:185], v[46:49]
	v_mfma_f32_16x16x32_bf16 v[34:37], v[154:157], v[186:189], v[34:37]
	v_mfma_f32_16x16x32_bf16 v[30:33], v[162:165], v[186:189], v[30:33]
	v_mfma_f32_16x16x32_bf16 v[18:21], v[154:157], v[170:173], v[18:21]
	v_mfma_f32_16x16x32_bf16 v[14:17], v[162:165], v[170:173], v[14:17]
	s_setprio 0
	s_setprio 1
	v_mfma_f32_16x16x32_bf16 v[58:61], v[134:137], v[190:193], v[58:61]
	v_mfma_f32_16x16x32_bf16 v[54:57], v[142:145], v[190:193], v[54:57]
	v_mfma_f32_16x16x32_bf16 v[42:45], v[134:137], v[178:181], v[42:45]
	v_mfma_f32_16x16x32_bf16 v[38:41], v[142:145], v[178:181], v[38:41]
	v_mfma_f32_16x16x32_bf16 v[26:29], v[134:137], v[174:177], v[26:29]
	v_mfma_f32_16x16x32_bf16 v[22:25], v[142:145], v[174:177], v[22:25]
	v_mfma_f32_16x16x32_bf16 v[10:13], v[134:137], v[166:169], v[10:13]
	v_mfma_f32_16x16x32_bf16 v[6:9], v[142:145], v[166:169], v[6:9]
	v_mfma_f32_16x16x32_bf16 v[58:61], v[138:141], v[194:197], v[58:61]
	v_mfma_f32_16x16x32_bf16 v[54:57], v[146:149], v[194:197], v[54:57]
	v_mfma_f32_16x16x32_bf16 v[42:45], v[138:141], v[182:185], v[42:45]
	v_mfma_f32_16x16x32_bf16 v[38:41], v[146:149], v[182:185], v[38:41]
	v_mfma_f32_16x16x32_bf16 v[26:29], v[138:141], v[186:189], v[26:29]
	v_mfma_f32_16x16x32_bf16 v[22:25], v[146:149], v[186:189], v[22:25]
	v_mfma_f32_16x16x32_bf16 v[10:13], v[138:141], v[170:173], v[10:13]
	v_mfma_f32_16x16x32_bf16 v[6:9], v[146:149], v[170:173], v[6:9]
	s_setprio 0
.LBB0_1012:
	v_cndmask_b32_e64 v213, v214, v215, s[6:7]
	v_cndmask_b32_e64 v225, v216, v217, s[6:7]
	s_bitcmp1_b32 s2, 0
	s_cbranch_scc0 .Lsb_guL0_4
	s_barrier
.Lsb_guL0_4:
	s_add_i32 s6, 0, 0x18000
	v_add_u32_e32 v134, s6, v226
	v_add_u32_e32 v135, s6, v227
	ds_read_b128 v[150:153], v134
	ds_read_b128 v[154:157], v135
	v_add_u32_e32 v134, s58, v226
	s_add_i32 s6, 0, 0x1c000
	v_add_u32_e32 v135, s58, v227
	ds_read_b128 v[158:161], v134
	ds_read_b128 v[162:165], v135
	v_add_u32_e32 v134, s6, v226
	v_add_u32_e32 v138, s6, v227
	v_add_u32_e32 v142, s59, v226
	v_add_u32_e32 v146, s59, v227
	ds_read_b128 v[134:137], v134
	ds_read_b128 v[138:141], v138
	ds_read_b128 v[142:145], v142
	ds_read_b128 v[146:149], v146
	s_mov_b32 m0, s42
	s_waitcnt lgkmcnt(0)
	ds_read_b128 v[190:193], v228 offset:32768
	ds_read_b128 v[178:181], v228 offset:34816
	ds_read_b128 v[194:197], v229 offset:32768
	ds_read_b128 v[182:185], v229 offset:34816
	ds_read_b128 v[174:177], v228 offset:36864
	ds_read_b128 v[166:169], v228 offset:38912
	ds_read_b128 v[186:189], v229 offset:36864
	ds_read_b128 v[170:173], v229 offset:38912
	global_load_lds_dwordx4 v213, s[34:35]
	s_mov_b32 m0, s43
	s_and_b64 vcc, exec, s[8:9]
	global_load_lds_dwordx4 v225, s[34:35]
	s_waitcnt vmcnt(8)
	s_waitcnt lgkmcnt(0)
	s_bitcmp0_b32 s2, 0
	s_cbranch_scc0 .Lsb_guL0_5
	s_barrier

; #define PG8_STAGE(bufoff, gbase, voff) do { _Pragma("unroll") for (int _i = 0; _i < 2; ++_i) \
;         __builtin_amdgcn_global_load_lds((const unsigned*)((const char*)(gbase) + (voff)[_i]), (LAS unsigned*)(lds + (bufoff) + ldsw + _i * 8192), 16, 0, 0); } while (0)
; #define PG8_LDA(dst, b, h) do { _Pragma("unroll") for (int m = 0; m < 4; ++m) _Pragma("unroll") for (int k = 0; k < 2; ++k) dst[m][k] = *(const LAS bf16x8*)(lds + PG8_SA(b, h) + ((aoff ^ (k * 64)) + m * 2048)); } while (0)
; #define PG8_MMA(ai, bj, At, Bt) do { __builtin_amdgcn_s_setprio(1); _Pragma("unroll") for (int m = 0; m < 4; ++m) _Pragma("unroll") for (int n = 0; n < 2; ++n) _Pragma("unroll") for (int k = 0; k < 2; ++k) \
;         acc[ai][bj][m][n] = __builtin_amdgcn_mfma_f32_16x16x32_bf16(Bt[n][k], At[m][k], acc[ai][bj][m][n], 0, 0, 0); __builtin_amdgcn_s_setprio(0); } while (0)
; #define PG8_WAIT_V(n) asm volatile("s_waitcnt vmcnt(" #n ")" ::: "memory")
; #define PG8_WAIT_L(n) asm volatile("s_waitcnt lgkmcnt(" #n ")" ::: "memory")
; #define PG8_BAR __builtin_amdgcn_s_barrier()
; #define PG8_SCHED __builtin_amdgcn_sched_barrier(0)
;     ...
;             PG8_LDA(At, 1, 1); PG8_STAGE(PG8_SB(1, 0), b3, voffB); PG8_STAGE(PG8_SB(1, 1), b3 + hstep, voffB); PG8_STAGE(PG8_SA(1, 0), a3, vs[0]);
;             PG8_WAIT_V(8); PG8_WAIT_L(0); PG8_BAR; if (do1) { PG8_MMA(1, 0, At, B0); PG8_MMA(1, 1, At, B1); } PG8_BAR; PG8_SCHED;
;         }
.LBB0_1014:
	v_mov_b32_e32 v225, v3
	s_add_u32 s6, s30, 0x4000
	v_lshl_add_u64 v[232:233], s[34:35], 0, v[2:3]
	v_lshl_add_u64 v[224:225], s[34:35], 0, v[224:225]
	s_addc_u32 s7, s31, 0
	s_bitcmp1_b32 s2, 0
	s_cbranch_scc0 .Lsb_guL0_6
	s_barrier
.Lsb_guL0_6:
	s_mov_b32 m0, s47
	v_lshl_add_u64 v[234:235], s[6:7], 0, v[202:203]
	s_waitcnt lgkmcnt(0)
	ds_read_b128 v[190:193], v228 offset:49152
	ds_read_b128 v[178:181], v228 offset:51200
	ds_read_b128 v[194:197], v229 offset:49152
	ds_read_b128 v[182:185], v229 offset:51200
	ds_read_b128 v[174:177], v228 offset:53248
	ds_read_b128 v[166:169], v228 offset:55296
	ds_read_b128 v[186:189], v229 offset:53248
	ds_read_b128 v[170:173], v229 offset:55296
	global_load_lds_dwordx4 v[234:235], off
	v_lshl_add_u64 v[234:235], s[6:7], 0, v[204:205]
	s_add_u32 s6, s30, 0x44000
	s_mov_b32 m0, s48
	s_addc_u32 s7, s31, 0
	global_load_lds_dwordx4 v[234:235], off
	v_lshl_add_u64 v[234:235], s[6:7], 0, v[202:203]
	s_mov_b32 m0, s51
	v_lshl_add_u64 v[232:233], v[232:233], 0, s[16:17]
	global_load_lds_dwordx4 v[234:235], off
	v_lshl_add_u64 v[234:235], s[6:7], 0, v[204:205]
	s_mov_b32 m0, s52
	v_lshl_add_u64 v[224:225], v[224:225], 0, s[16:17]
	global_load_lds_dwordx4 v[234:235], off
	s_mov_b32 m0, s49
	s_and_b64 vcc, exec, s[10:11]
	global_load_lds_dwordx4 v[232:233], off
	s_mov_b32 m0, s50
	s_nop 0
	global_load_lds_dwordx4 v[224:225], off
	s_waitcnt vmcnt(8)
	s_waitcnt lgkmcnt(0)
	s_bitcmp0_b32 s2, 0
	s_cbranch_scc0 .Lsb_guL0_7
	s_barrier
.Lsb_guL0_7:
	s_cbranch_vccnz .LBB0_1005
	s_setprio 1
	s_waitcnt lgkmcnt(0)
	v_mfma_f32_16x16x32_bf16 v[66:69], v[150:153], v[190:193], v[66:69]
	v_mfma_f32_16x16x32_bf16 v[62:65], v[158:161], v[190:193], v[62:65]
	v_mfma_f32_16x16x32_bf16 v[50:53], v[150:153], v[178:181], v[50:53]
	v_mfma_f32_16x16x32_bf16 v[46:49], v[158:161], v[178:181], v[46:49]
	v_mfma_f32_16x16x32_bf16 v[34:37], v[150:153], v[174:177], v[34:37]
	v_mfma_f32_16x16x32_bf16 v[30:33], v[158:161], v[174:177], v[30:33]
	v_mfma_f32_16x16x32_bf16 v[18:21], v[150:153], v[166:169], v[18:21]
	v_mfma_f32_16x16x32_bf16 v[14:17], v[158:161], v[166:169], v[14:17]
	v_mfma_f32_16x16x32_bf16 v[66:69], v[154:157], v[194:197], v[66:69]
	v_mfma_f32_16x16x32_bf16 v[62:65], v[162:165], v[194:197], v[62:65]
	v_mfma_f32_16x16x32_bf16 v[50:53], v[154:157], v[182:185], v[50:53]
	v_mfma_f32_16x16x32_bf16 v[46:49], v[162:165], v[182:185], v[46:49]
	v_mfma_f32_16x16x32_bf16 v[34:37], v[154:157], v[186:189], v[34:37]
	v_mfma_f32_16x16x32_bf16 v[30:33], v[162:165], v[186:189], v[30:33]
	v_mfma_f32_16x16x32_bf16 v[18:21], v[154:157], v[170:173], v[18:21]
	v_mfma_f32_16x16x32_bf16 v[14:17], v[162:165], v[170:173], v[14:17]
	s_setprio 0
	s_setprio 1
	v_mfma_f32_16x16x32_bf16 v[58:61], v[134:137], v[190:193], v[58:61]
	v_mfma_f32_16x16x32_bf16 v[54:57], v[142:145], v[190:193], v[54:57]
	v_mfma_f32_16x16x32_bf16 v[42:45], v[134:137], v[178:181], v[42:45]
	v_mfma_f32_16x16x32_bf16 v[38:41], v[142:145], v[178:181], v[38:41]
	v_mfma_f32_16x16x32_bf16 v[26:29], v[134:137], v[174:177], v[26:29]
	v_mfma_f32_16x16x32_bf16 v[22:25], v[142:145], v[174:177], v[22:25]
	v_mfma_f32_16x16x32_bf16 v[10:13], v[134:137], v[166:169], v[10:13]
	v_mfma_f32_16x16x32_bf16 v[6:9], v[142:145], v[166:169], v[6:9]
	v_mfma_f32_16x16x32_bf16 v[58:61], v[138:141], v[194:197], v[58:61]
	v_mfma_f32_16x16x32_bf16 v[54:57], v[146:149], v[194:197], v[54:57]
	v_mfma_f32_16x16x32_bf16 v[42:45], v[138:141], v[182:185], v[42:45]
	v_mfma_f32_16x16x32_bf16 v[38:41], v[146:149], v[182:185], v[38:41]
	v_mfma_f32_16x16x32_bf16 v[26:29], v[138:141], v[186:189], v[26:29]
	v_mfma_f32_16x16x32_bf16 v[22:25], v[146:149], v[186:189], v[22:25]
	v_mfma_f32_16x16x32_bf16 v[10:13], v[138:141], v[170:173], v[10:13]
	v_mfma_f32_16x16x32_bf16 v[6:9], v[146:149], v[170:173], v[6:9]
	s_setprio 0
	s_branch .LBB0_1005

; __device__ __forceinline__ float silu_fast(float v) { return v * __builtin_amdgcn_rcpf(1.f + __builtin_amdgcn_exp2f(-1.4426950408889634f * v)); }
; __device__ __forceinline__ u32x4 pack8(const f32x4 a, const f32x4 b) { u32x4 w; w.x = cvt_pk_bf16(a[0], a[1]); w.y = cvt_pk_bf16(a[2], a[3]); w.z = cvt_pk_bf16(b[0], b[1]); w.w = cvt_pk_bf16(b[2], b[3]); return w; }
; #define PG8_BAR __builtin_amdgcn_s_barrier()
;     __device__ __forceinline__ void operator()(const f32x4 (&acc)[2][2][4][2], const Unit& u, int wr, int wc, int fr, int fq) const {
;         const int row0 = u.pm * BM + wr * 64 + fr, col0 = u.pn * HALF + wc * 32 + 8 * fq;
;         bf16_t* base = HID + (size_t)u.z * MEXP * FF;
; #pragma unroll
;         for (int ai = 0; ai < 2; ++ai)
; #pragma unroll
;             for (int m = 0; m < 4; ++m) { f32x4 h[2];
; #pragma unroll
;                 for (int n = 0; n < 2; ++n)
; #pragma unroll
;                     for (int j = 0; j < 4; ++j) h[n][j] = silu_fast(acc[ai][0][m][n][j]) * acc[ai][1][m][n][j];
;                 const int row = row0 + ai * HALF + m * 16;
;                 *(u32x4*)(base + ((size_t)(row >> 7) * (FF / 64) + (col0 >> 6)) * 8192 + (row & 127) * 64 + (col0 & 63)) = pack8(h[0], h[1]); }
;     ...
;         if (wr == 0) PG8_BAR;
.LBB0_1018:
	v_mul_f32_e32 v2, 0xbfb8aa3b, v130
	v_exp_f32_e32 v2, v2
	v_mul_f32_e32 v136, 0xbfb8aa3b, v131
	v_exp_f32_e32 v136, v136
	s_lshl_b32 s6, s63, 8
	v_add_f32_e32 v2, 1.0, v2
	v_rcp_f32_e32 v138, v2
	v_add_f32_e32 v2, 1.0, v136
	v_rcp_f32_e32 v139, v2
	v_mul_f32_e32 v2, 0xbfb8aa3b, v132
	v_exp_f32_e32 v2, v2
	s_add_i32 s6, s6, s45
	v_pk_mul_f32 v[130:131], v[130:131], v[138:139]
	v_mul_f32_e32 v138, 0xbfb8aa3b, v133
	v_exp_f32_e32 v138, v138
	v_add_f32_e32 v2, 1.0, v2
	v_pk_mul_f32 v[122:123], v[122:123], v[130:131]
	v_rcp_f32_e32 v130, v2
	v_add_f32_e32 v2, 1.0, v138
	v_rcp_f32_e32 v131, v2
	v_mul_f32_e32 v2, 0xbfb8aa3b, v126
	v_exp_f32_e32 v2, v2
	v_mul_f32_e32 v138, 0xbfb8aa3b, v127
	v_exp_f32_e32 v138, v138
	v_pk_mul_f32 v[130:131], v[132:133], v[130:131]
	v_add_f32_e32 v2, 1.0, v2
	v_mul_f32_e32 v133, 0xbfb8aa3b, v128
	v_rcp_f32_e32 v132, v2
	v_add_f32_e32 v2, 1.0, v138
	v_exp_f32_e32 v138, v133
	v_mul_f32_e32 v133, 0xbfb8aa3b, v129
	v_exp_f32_e32 v139, v133
	v_rcp_f32_e32 v133, v2
	v_add_f32_e32 v2, 1.0, v138
	v_rcp_f32_e32 v138, v2
	v_add_f32_e32 v2, 1.0, v139
	v_rcp_f32_e32 v139, v2
	s_lshl_b32 s4, s22, 7
	v_pk_mul_f32 v[126:127], v[126:127], v[132:133]
	s_or_b32 s4, s4, s46
	s_ashr_i32 s7, s6, 7
	v_pk_mul_f32 v[126:127], v[118:119], v[126:127]
	v_pk_mul_f32 v[118:119], v[128:129], v[138:139]
	v_mul_f32_e32 v2, 0xbfb8aa3b, v114
	s_ashr_i32 s5, s4, 6
	v_mad_i64_i32 v[134:135], s[8:9], s62, v230, v[206:207]
	s_mul_i32 s7, s7, 44
	v_pk_mul_f32 v[128:129], v[120:121], v[118:119]
	v_exp_f32_e32 v2, v2
	v_mul_f32_e32 v121, 0xbfb8aa3b, v115
	s_ashr_i32 s4, s5, 31
	s_ashr_i32 s9, s7, 31
	v_cvt_pk_bf16_f32 v118, v122, v123
	v_exp_f32_e32 v123, v121
	s_add_u32 s8, s7, s5
	s_addc_u32 s9, s9, s4
	s_lshl_b64 s[8:9], s[8:9], 14
	v_add_f32_e32 v2, 1.0, v2
	v_lshl_add_u64 v[136:137], v[134:135], 0, s[8:9]
	v_pk_mul_f32 v[124:125], v[124:125], v[130:131]
	v_rcp_f32_e32 v122, v2
	v_add_f32_e32 v2, 1.0, v123
	v_mov_b32_e32 v209, v3
	v_cvt_pk_bf16_f32 v119, v124, v125
	v_cvt_pk_bf16_f32 v120, v126, v127
	v_cvt_pk_bf16_f32 v121, v128, v129
	v_rcp_f32_e32 v123, v2
	v_lshl_add_u64 v[124:125], v[136:137], 0, v[208:209]
	v_mul_f32_e32 v2, 0xbfb8aa3b, v116
	global_store_dwordx4 v[124:125], v[118:121], off
	v_exp_f32_e32 v2, v2
	v_pk_mul_f32 v[114:115], v[114:115], v[122:123]
	v_mul_f32_e32 v118, 0xbfb8aa3b, v117
	v_exp_f32_e32 v118, v118
	v_add_f32_e32 v2, 1.0, v2
	v_pk_mul_f32 v[106:107], v[106:107], v[114:115]
	v_rcp_f32_e32 v114, v2
	v_add_f32_e32 v2, 1.0, v118
	v_rcp_f32_e32 v115, v2
	v_mul_f32_e32 v2, 0xbfb8aa3b, v110
	v_exp_f32_e32 v2, v2
	v_mul_f32_e32 v118, 0xbfb8aa3b, v111
	v_exp_f32_e32 v118, v118
	v_pk_mul_f32 v[114:115], v[116:117], v[114:115]
	v_add_f32_e32 v2, 1.0, v2
	v_mul_f32_e32 v117, 0xbfb8aa3b, v112
	v_rcp_f32_e32 v116, v2
	v_add_f32_e32 v2, 1.0, v118
	v_exp_f32_e32 v118, v117
	v_mul_f32_e32 v117, 0xbfb8aa3b, v113
	v_exp_f32_e32 v119, v117
	v_rcp_f32_e32 v117, v2
	v_add_f32_e32 v2, 1.0, v118
	v_rcp_f32_e32 v118, v2
	v_add_f32_e32 v2, 1.0, v119
	v_rcp_f32_e32 v119, v2
	v_pk_mul_f32 v[110:111], v[110:111], v[116:117]
	v_mul_f32_e32 v2, 0xbfb8aa3b, v98
	v_pk_mul_f32 v[110:111], v[102:103], v[110:111]
	v_pk_mul_f32 v[102:103], v[112:113], v[118:119]
	v_exp_f32_e32 v2, v2
	v_pk_mul_f32 v[112:113], v[104:105], v[102:103]
	v_mul_f32_e32 v103, 0xbfb8aa3b, v99
	v_exp_f32_e32 v104, v103
	v_add_f32_e32 v2, 1.0, v2
	v_pk_mul_f32 v[108:109], v[108:109], v[114:115]
	v_cvt_pk_bf16_f32 v102, v106, v107
	v_rcp_f32_e32 v106, v2
	v_add_f32_e32 v2, 1.0, v104
	v_cvt_pk_bf16_f32 v103, v108, v109
	v_rcp_f32_e32 v107, v2
	v_cvt_pk_bf16_f32 v104, v110, v111
	v_cvt_pk_bf16_f32 v105, v112, v113
	v_mul_f32_e32 v2, 0xbfb8aa3b, v100
	global_store_dwordx4 v[124:125], v[102:105], off offset:2048
	v_exp_f32_e32 v2, v2
	v_pk_mul_f32 v[98:99], v[98:99], v[106:107]
	v_mul_f32_e32 v102, 0xbfb8aa3b, v101
	v_exp_f32_e32 v102, v102
	v_add_f32_e32 v2, 1.0, v2
	v_pk_mul_f32 v[90:91], v[90:91], v[98:99]
	v_rcp_f32_e32 v98, v2
	v_add_f32_e32 v2, 1.0, v102
	v_rcp_f32_e32 v99, v2
	v_mul_f32_e32 v2, 0xbfb8aa3b, v94
	v_exp_f32_e32 v2, v2
	v_mul_f32_e32 v102, 0xbfb8aa3b, v95
	v_exp_f32_e32 v102, v102
	v_pk_mul_f32 v[98:99], v[100:101], v[98:99]
	v_add_f32_e32 v2, 1.0, v2
	v_mul_f32_e32 v101, 0xbfb8aa3b, v96
	v_rcp_f32_e32 v100, v2
	v_add_f32_e32 v2, 1.0, v102
	v_exp_f32_e32 v102, v101
	v_mul_f32_e32 v101, 0xbfb8aa3b, v97
	v_exp_f32_e32 v103, v101
	v_rcp_f32_e32 v101, v2
	v_add_f32_e32 v2, 1.0, v102
	v_rcp_f32_e32 v102, v2
	v_add_f32_e32 v2, 1.0, v103
	v_rcp_f32_e32 v103, v2
	v_pk_mul_f32 v[94:95], v[94:95], v[100:101]
	v_mul_f32_e32 v2, 0xbfb8aa3b, v82
	v_pk_mul_f32 v[94:95], v[86:87], v[94:95]
	v_pk_mul_f32 v[86:87], v[96:97], v[102:103]
	v_exp_f32_e32 v2, v2
	v_pk_mul_f32 v[96:97], v[88:89], v[86:87]
	v_mul_f32_e32 v89, 0xbfb8aa3b, v83
	v_cvt_pk_bf16_f32 v86, v90, v91
	v_exp_f32_e32 v91, v89
	v_add_f32_e32 v2, 1.0, v2
	v_pk_mul_f32 v[92:93], v[92:93], v[98:99]
	v_rcp_f32_e32 v90, v2
	v_add_f32_e32 v2, 1.0, v91
	v_mov_b32_e32 v211, v3
	v_cvt_pk_bf16_f32 v87, v92, v93
	v_cvt_pk_bf16_f32 v88, v94, v95
	v_cvt_pk_bf16_f32 v89, v96, v97
	v_rcp_f32_e32 v91, v2
	v_lshl_add_u64 v[92:93], v[136:137], 0, v[210:211]
	v_mul_f32_e32 v2, 0xbfb8aa3b, v84
	global_store_dwordx4 v[92:93], v[86:89], off
	v_exp_f32_e32 v2, v2
	v_pk_mul_f32 v[82:83], v[82:83], v[90:91]
	v_mul_f32_e32 v86, 0xbfb8aa3b, v85
	v_exp_f32_e32 v86, v86
	v_add_f32_e32 v2, 1.0, v2
	v_pk_mul_f32 v[74:75], v[74:75], v[82:83]
	v_rcp_f32_e32 v82, v2
	v_add_f32_e32 v2, 1.0, v86
	v_rcp_f32_e32 v83, v2
	v_mul_f32_e32 v2, 0xbfb8aa3b, v78
	v_exp_f32_e32 v2, v2
	v_mul_f32_e32 v86, 0xbfb8aa3b, v79
	v_exp_f32_e32 v86, v86
; __device__ __forceinline__ float silu_fast(float v) { return v * __builtin_amdgcn_rcpf(1.f + __builtin_amdgcn_exp2f(-1.4426950408889634f * v)); }
; __device__ __forceinline__ u32x4 pack8(const f32x4 a, const f32x4 b) { u32x4 w; w.x = cvt_pk_bf16(a[0], a[1]); w.y = cvt_pk_bf16(a[2], a[3]); w.z = cvt_pk_bf16(b[0], b[1]); w.w = cvt_pk_bf16(b[2], b[3]); return w; }
; #define PG8_BAR __builtin_amdgcn_s_barrier()
;     __device__ __forceinline__ void operator()(const f32x4 (&acc)[2][2][4][2], const Unit& u, int wr, int wc, int fr, int fq) const {
;     ...
;             for (int m = 0; m < 4; ++m) { f32x4 h[2];
; #pragma unroll
;                 for (int n = 0; n < 2; ++n)
; #pragma unroll
;                     for (int j = 0; j < 4; ++j) h[n][j] = silu_fast(acc[ai][0][m][n][j]) * acc[ai][1][m][n][j];
;                 const int row = row0 + ai * HALF + m * 16;
;                 *(u32x4*)(base + ((size_t)(row >> 7) * (FF / 64) + (col0 >> 6)) * 8192 + (row & 127) * 64 + (col0 & 63)) = pack8(h[0], h[1]); }
;     ...
;         if (!has_next) break;
; #pragma unroll
;         for (int a = 0; a < 2; ++a)
; #pragma unroll
;             for (int b = 0; b < 2; ++b)
; #pragma unroll
;                 for (int m = 0; m < 4; ++m)
; #pragma unroll
;                     for (int n = 0; n < 2; ++n) acc[a][b][m][n] = (f32x4){0.f, 0.f, 0.f, 0.f};
;         cur = nxt; cA = nA; cB = nB; ++ui;
; #pragma unroll
;         for (int hh = 0; hh < 2; ++hh)
; #pragma unroll
;             for (int i = 0; i < 2; ++i) voffA[hh][i] = voffN[hh][i];
;         if (wr == 1) PG8_BAR;
	v_pk_mul_f32 v[82:83], v[84:85], v[82:83]
	v_add_f32_e32 v2, 1.0, v2
	v_mul_f32_e32 v85, 0xbfb8aa3b, v80
	v_rcp_f32_e32 v84, v2
	v_add_f32_e32 v2, 1.0, v86
	v_exp_f32_e32 v86, v85
	v_mul_f32_e32 v85, 0xbfb8aa3b, v81
	v_exp_f32_e32 v87, v85
	v_rcp_f32_e32 v85, v2
	v_add_f32_e32 v2, 1.0, v86
	v_rcp_f32_e32 v86, v2
	v_add_f32_e32 v2, 1.0, v87
	v_rcp_f32_e32 v87, v2
	v_pk_mul_f32 v[78:79], v[78:79], v[84:85]
	v_pk_mul_f32 v[76:77], v[76:77], v[82:83]
	v_pk_mul_f32 v[78:79], v[70:71], v[78:79]
	v_pk_mul_f32 v[70:71], v[80:81], v[86:87]
	v_mov_b32_e32 v213, v3
	v_pk_mul_f32 v[80:81], v[72:73], v[70:71]
	v_cvt_pk_bf16_f32 v70, v74, v75
	v_cvt_pk_bf16_f32 v71, v76, v77
	v_cvt_pk_bf16_f32 v72, v78, v79
	v_cvt_pk_bf16_f32 v73, v80, v81
	v_lshl_add_u64 v[74:75], v[136:137], 0, v[212:213]
	v_mul_f32_e32 v2, 0xbfb8aa3b, v66
	global_store_dwordx4 v[74:75], v[70:73], off
	v_exp_f32_e32 v2, v2
	s_addk_i32 s6, 0x80
	v_mul_f32_e32 v70, 0xbfb8aa3b, v67
	v_exp_f32_e32 v70, v70
	v_add_f32_e32 v2, 1.0, v2
	v_rcp_f32_e32 v72, v2
	s_ashr_i32 s6, s6, 7
	v_add_f32_e32 v2, 1.0, v70
	v_rcp_f32_e32 v73, v2
	v_mul_f32_e32 v2, 0xbfb8aa3b, v68
	v_exp_f32_e32 v2, v2
	s_mul_i32 s6, s6, 44
	v_pk_mul_f32 v[66:67], v[66:67], v[72:73]
	v_mul_f32_e32 v72, 0xbfb8aa3b, v69
	v_exp_f32_e32 v72, v72
	v_add_f32_e32 v2, 1.0, v2
	v_pk_mul_f32 v[58:59], v[58:59], v[66:67]
	v_rcp_f32_e32 v66, v2
	v_add_f32_e32 v2, 1.0, v72
	v_rcp_f32_e32 v67, v2
	v_mul_f32_e32 v2, 0xbfb8aa3b, v62
	v_exp_f32_e32 v2, v2
	v_mul_f32_e32 v72, 0xbfb8aa3b, v63
	v_exp_f32_e32 v72, v72
	v_pk_mul_f32 v[66:67], v[68:69], v[66:67]
	v_add_f32_e32 v2, 1.0, v2
	v_mul_f32_e32 v69, 0xbfb8aa3b, v64
	v_rcp_f32_e32 v68, v2
	v_add_f32_e32 v2, 1.0, v72
	v_exp_f32_e32 v72, v69
	v_mul_f32_e32 v69, 0xbfb8aa3b, v65
	v_exp_f32_e32 v73, v69
	v_rcp_f32_e32 v69, v2
	v_add_f32_e32 v2, 1.0, v72
	v_rcp_f32_e32 v72, v2
	v_add_f32_e32 v2, 1.0, v73
	v_rcp_f32_e32 v73, v2
	v_pk_mul_f32 v[62:63], v[62:63], v[68:69]
	v_mul_f32_e32 v2, 0xbfb8aa3b, v50
	v_pk_mul_f32 v[62:63], v[54:55], v[62:63]
	v_pk_mul_f32 v[54:55], v[64:65], v[72:73]
	v_exp_f32_e32 v2, v2
	v_pk_mul_f32 v[64:65], v[56:57], v[54:55]
	v_mul_f32_e32 v56, 0xbfb8aa3b, v51
	s_ashr_i32 s7, s6, 31
	v_exp_f32_e32 v57, v56
	s_add_u32 s6, s6, s5
	s_addc_u32 s7, s7, s4
	s_lshl_b64 s[4:5], s[6:7], 14
	v_add_f32_e32 v2, 1.0, v2
	v_lshl_add_u64 v[70:71], v[134:135], 0, s[4:5]
	v_pk_mul_f32 v[60:61], v[60:61], v[66:67]
	v_cvt_pk_bf16_f32 v54, v58, v59
	v_rcp_f32_e32 v58, v2
	v_add_f32_e32 v2, 1.0, v57
	v_cvt_pk_bf16_f32 v55, v60, v61
	v_cvt_pk_bf16_f32 v56, v62, v63
	v_rcp_f32_e32 v59, v2
	v_cvt_pk_bf16_f32 v57, v64, v65
	v_lshl_add_u64 v[60:61], v[70:71], 0, v[208:209]
	v_mul_f32_e32 v2, 0xbfb8aa3b, v52
	global_store_dwordx4 v[60:61], v[54:57], off
	v_exp_f32_e32 v2, v2
	v_pk_mul_f32 v[50:51], v[50:51], v[58:59]
	v_mul_f32_e32 v54, 0xbfb8aa3b, v53
	v_exp_f32_e32 v54, v54
	v_add_f32_e32 v2, 1.0, v2
	v_pk_mul_f32 v[42:43], v[42:43], v[50:51]
	v_rcp_f32_e32 v50, v2
	v_add_f32_e32 v2, 1.0, v54
	v_rcp_f32_e32 v51, v2
	v_mul_f32_e32 v2, 0xbfb8aa3b, v46
	v_exp_f32_e32 v2, v2
	v_mul_f32_e32 v54, 0xbfb8aa3b, v47
	v_exp_f32_e32 v54, v54
	v_pk_mul_f32 v[50:51], v[52:53], v[50:51]
	v_add_f32_e32 v2, 1.0, v2
	v_mul_f32_e32 v53, 0xbfb8aa3b, v48
	v_rcp_f32_e32 v52, v2
	v_add_f32_e32 v2, 1.0, v54
	v_exp_f32_e32 v54, v53
	v_mul_f32_e32 v53, 0xbfb8aa3b, v49
	v_exp_f32_e32 v55, v53
	v_rcp_f32_e32 v53, v2
	v_add_f32_e32 v2, 1.0, v54
	v_rcp_f32_e32 v54, v2
	v_add_f32_e32 v2, 1.0, v55
	v_rcp_f32_e32 v55, v2
	v_pk_mul_f32 v[46:47], v[46:47], v[52:53]
	v_mul_f32_e32 v2, 0xbfb8aa3b, v34
	v_pk_mul_f32 v[46:47], v[38:39], v[46:47]
	v_pk_mul_f32 v[38:39], v[48:49], v[54:55]
	v_exp_f32_e32 v2, v2
	v_pk_mul_f32 v[48:49], v[40:41], v[38:39]
	v_mul_f32_e32 v39, 0xbfb8aa3b, v35
	v_exp_f32_e32 v40, v39
	v_add_f32_e32 v2, 1.0, v2
	v_pk_mul_f32 v[44:45], v[44:45], v[50:51]
	v_cvt_pk_bf16_f32 v38, v42, v43
	v_rcp_f32_e32 v42, v2
	v_add_f32_e32 v2, 1.0, v40
	v_cvt_pk_bf16_f32 v39, v44, v45
	v_rcp_f32_e32 v43, v2
	v_cvt_pk_bf16_f32 v40, v46, v47
	v_cvt_pk_bf16_f32 v41, v48, v49
	v_mul_f32_e32 v2, 0xbfb8aa3b, v36
	global_store_dwordx4 v[60:61], v[38:41], off offset:2048
	v_exp_f32_e32 v2, v2
	v_pk_mul_f32 v[34:35], v[34:35], v[42:43]
	v_mul_f32_e32 v38, 0xbfb8aa3b, v37
	v_exp_f32_e32 v38, v38
	v_add_f32_e32 v2, 1.0, v2
	v_pk_mul_f32 v[26:27], v[26:27], v[34:35]
	v_rcp_f32_e32 v34, v2
	v_add_f32_e32 v2, 1.0, v38
	v_rcp_f32_e32 v35, v2
	v_mul_f32_e32 v2, 0xbfb8aa3b, v30
	v_exp_f32_e32 v2, v2
	v_mul_f32_e32 v38, 0xbfb8aa3b, v31
	v_exp_f32_e32 v38, v38
	v_pk_mul_f32 v[34:35], v[36:37], v[34:35]
	v_add_f32_e32 v2, 1.0, v2
	v_mul_f32_e32 v37, 0xbfb8aa3b, v32
	v_rcp_f32_e32 v36, v2
	v_add_f32_e32 v2, 1.0, v38
	v_exp_f32_e32 v38, v37
	v_mul_f32_e32 v37, 0xbfb8aa3b, v33
	v_exp_f32_e32 v39, v37
	v_rcp_f32_e32 v37, v2
	v_add_f32_e32 v2, 1.0, v38
	v_rcp_f32_e32 v38, v2
	v_add_f32_e32 v2, 1.0, v39
	v_rcp_f32_e32 v39, v2
	v_pk_mul_f32 v[30:31], v[30:31], v[36:37]
	v_mul_f32_e32 v2, 0xbfb8aa3b, v18
	v_pk_mul_f32 v[30:31], v[22:23], v[30:31]
	v_pk_mul_f32 v[22:23], v[32:33], v[38:39]
	v_exp_f32_e32 v2, v2
	v_pk_mul_f32 v[32:33], v[24:25], v[22:23]
	v_mul_f32_e32 v24, 0xbfb8aa3b, v19
	v_exp_f32_e32 v25, v24
	v_add_f32_e32 v2, 1.0, v2
	v_pk_mul_f32 v[28:29], v[28:29], v[34:35]
	v_cvt_pk_bf16_f32 v22, v26, v27
	v_rcp_f32_e32 v26, v2
	v_add_f32_e32 v2, 1.0, v25
	v_cvt_pk_bf16_f32 v23, v28, v29
	v_cvt_pk_bf16_f32 v24, v30, v31
	v_rcp_f32_e32 v27, v2
	v_cvt_pk_bf16_f32 v25, v32, v33
	v_lshl_add_u64 v[28:29], v[70:71], 0, v[210:211]
	v_mul_f32_e32 v2, 0xbfb8aa3b, v20
	global_store_dwordx4 v[28:29], v[22:25], off
	v_exp_f32_e32 v2, v2
	v_pk_mul_f32 v[18:19], v[18:19], v[26:27]
	v_mul_f32_e32 v22, 0xbfb8aa3b, v21
	v_exp_f32_e32 v22, v22
	v_add_f32_e32 v2, 1.0, v2
	v_pk_mul_f32 v[10:11], v[10:11], v[18:19]
	v_rcp_f32_e32 v18, v2
	v_add_f32_e32 v2, 1.0, v22
	v_rcp_f32_e32 v19, v2
	v_mul_f32_e32 v2, 0xbfb8aa3b, v14
	v_exp_f32_e32 v2, v2
	v_mul_f32_e32 v22, 0xbfb8aa3b, v15
	v_exp_f32_e32 v22, v22
	v_pk_mul_f32 v[18:19], v[20:21], v[18:19]
	v_add_f32_e32 v2, 1.0, v2
	v_mul_f32_e32 v21, 0xbfb8aa3b, v16
	v_rcp_f32_e32 v20, v2
	v_add_f32_e32 v2, 1.0, v22
	v_exp_f32_e32 v22, v21
	v_mul_f32_e32 v21, 0xbfb8aa3b, v17
	v_exp_f32_e32 v23, v21
	v_rcp_f32_e32 v21, v2
	v_add_f32_e32 v2, 1.0, v22
	v_rcp_f32_e32 v22, v2
	v_add_f32_e32 v2, 1.0, v23
	v_rcp_f32_e32 v23, v2
	v_pk_mul_f32 v[14:15], v[14:15], v[20:21]
	v_pk_mul_f32 v[12:13], v[12:13], v[18:19]
	v_pk_mul_f32 v[14:15], v[6:7], v[14:15]
	v_pk_mul_f32 v[6:7], v[16:17], v[22:23]
	s_and_b64 vcc, exec, s[0:1]
	v_pk_mul_f32 v[16:17], v[8:9], v[6:7]
	v_cvt_pk_bf16_f32 v6, v10, v11
	v_cvt_pk_bf16_f32 v7, v12, v13
	v_cvt_pk_bf16_f32 v8, v14, v15
	v_cvt_pk_bf16_f32 v9, v16, v17
	v_lshl_add_u64 v[10:11], v[70:71], 0, v[212:213]
	s_mov_b64 s[0:1], -1
	global_store_dwordx4 v[10:11], v[6:9], off
	s_cbranch_vccnz .LBB0_999
	s_andn2_b64 vcc, exec, s[2:3]
	s_cbranch_vccnz .LBB0_998
	s_branch .LBB0_998

;     __device__ bool next(int i, Unit& u) const { return map((long)i * G + c, u); }
;     __device__ bool next(int i, Unit& u) const {
;         const int x = c & 7, j = (c >> 3) + i * (G >> 3), per = nM * nN;
;         if (j >= 2 * per) return false;
;         const int el = j / per, rem = j % per, grp = rem / (nM * GP), w = rem % (nM * GP);
;         u.kq = -1; u.z = 2 * x + el; u.pm = w % nM; u.pn = grp * GP + w / nM; return true;
;     ...
;     for (int i = 0; i < 2; ++i) { stage_rc(tid * 16 + i * 8192, sR[i], sC[i]); const int Rb = Epi::PERM ? ((sR[i] & ~31) + perm32(sR[i] & 31)) : sR[i];
;         voffB[i] = (TILED & 2) ? (unsigned)(Rb * BK + sC[i]) * 2u : (unsigned)(Rb * K + sC[i]) * 2u; }
;     constexpr size_t kstepA = (TILED & 1) ? (size_t)HALF * BK * 2 : (size_t)(BK * 2), kstepB = (TILED & 2) ? (size_t)HALF * BK * 2 : (size_t)(BK * 2);
;     const size_t hstep = (size_t)HALF * K * 2;
;     const size_t tstep = 2 * hstep;
;     const unsigned ldsw = (unsigned)wid * 1024u;
;     const int aoff = lds_byte(wr * 64 + fr, fq * 8), boff = lds_byte(wc * 32 + fr, fq * 8);
;     ...
;     Unit cur, nxt; int ui = 0;
;     if (!S.next(0, cur)) return;
;     if constexpr (GATHER) {
;         for (int k = tid >> 8;; k += 2) { Unit u; if (!S.next(k, u)) break; idxl[k * 256 + (tid & 255)] = g.ridx[(size_t)u.z * g.ridxStrideZ + u.pm * BM + (tid & 255)]; }
;         __syncthreads();
; #pragma unroll
;         for (int hh = 0; hh < 2; ++hh)
; #pragma unroll
;             for (int i = 0; i < 2; ++i) voffA[hh][i] = (unsigned)idxl[hh * HALF + sR[i]] * (unsigned)(K * 2) + (unsigned)sC[i] * 2u;
;     } else {
; #pragma unroll
;         for (int hh = 0; hh < 2; ++hh)
; #pragma unroll
;             for (int i = 0; i < 2; ++i) voffA[hh][i] = (TILED & 1) ? (unsigned)hh * (unsigned)(HALF * K * 2) + (unsigned)(sR[i] * BK + sC[i]) * 2u : (unsigned)((hh * HALF + sR[i]) * K + sC[i]) * 2u;
;     }
; #pragma unroll
;     for (int hh = 0; hh < 2; ++hh)
; #pragma unroll
;         for (int i = 0; i < 2; ++i) voffN[hh][i] = voffA[hh][i];
;     f32x4 acc[2][2][4][2];
; #pragma unroll
;     for (int a = 0; a < 2; ++a)
; #pragma unroll
;         for (int b = 0; b < 2; ++b)
; #pragma unroll
;             for (int m = 0; m < 4; ++m)
; #pragma unroll
;                 for (int n = 0; n < 2; ++n) acc[a][b][m][n] = (f32x4){0.f, 0.f, 0.f, 0.f};
;     bf16x8 At[4][2], B0[2][2], B1[2][2];
.LBB0_2327:
	s_or_b64 exec, exec, s[0:1]
	s_mul_hi_i32 s0, s75, 0x2e8ba2e9
	s_lshr_b32 s1, s0, 31
	s_ashr_i32 s0, s0, 5
	s_add_i32 s0, s0, s1
	s_mul_i32 s1, s0, 0xb0
	s_sub_i32 s1, s75, s1
	s_lshr_b32 s2, s1, 27
	s_and_b32 s2, s2, 15
	s_add_i32 s2, s1, s2
	v_ashrrev_i32_e32 v4, 31, v1
	s_sext_i32_i16 s3, s2
	s_and_b32 s2, s2, 0xfff0
	v_lshrrev_b32_e32 v4, 22, v4
	s_sub_i32 s1, s1, s2
	v_add_u32_e32 v4, v1, v4
	v_add_u32_e32 v2, 0x2000, v1
	s_add_i32 s51, s0, s28
	s_bfe_i32 s0, s1, 0x80000
	v_and_b32_e32 v4, 0xfc00, v4
	s_bfe_u32 s0, s0, 0x3000c
	v_sub_u32_e32 v1, v1, v4
	v_ashrrev_i32_e32 v4, 31, v2
	s_add_i32 s0, s1, s0
	v_lshrrev_b32_e32 v4, 22, v4
	s_ashr_i32 s3, s3, 4
	s_sext_i32_i8 s0, s0
	v_add_u32_e32 v4, v2, v4
	s_lshr_b32 s7, s0, 3
	s_lshl_b32 s2, s3, 1
	s_ashr_i32 s0, s0, 3
	v_ashrrev_i32_e32 v5, 10, v4
	v_and_b32_e32 v4, 0xfc00, v4
	s_add_i32 s16, s2, s0
	v_ashrrev_i32_e32 v3, 31, v6
	v_sub_u32_e32 v2, v2, v4
	s_mov_b32 s0, 0x5040100
	v_lshrrev_b32_e32 v3, 26, v3
	v_perm_b32 v1, v2, v1, s0
	v_add_u32_e32 v3, v6, v3
	v_pk_ashrrev_i16 v1, 4, v1 op_sel_hi:[0,1]
	v_mov_b32_e32 v4, 3
	v_ashrrev_i32_e32 v3, 6, v3
	v_ashrrev_i32_sdwa v4, v4, sext(v1) dst_sel:DWORD dst_unused:UNUSED_PAD src0_sel:DWORD src1_sel:WORD_0
	v_lshl_add_u32 v131, v3, 3, v4
	v_lshlrev_b32_e32 v3, 1, v131
	v_lshrrev_b32_e32 v7, 2, v131
	v_and_b32_e32 v8, 3, v4
	s_mov_b32 s0, 0x1ffffe0
	v_ashrrev_i32_e32 v2, 19, v1
	v_and_b32_e32 v3, 24, v3
	v_and_b32_e32 v7, 4, v7
	v_and_or_b32 v8, v131, s0, v8
	v_or3_b32 v3, v8, v7, v3
	v_xor_b32_sdwa v7, v2, sext(v1) dst_sel:DWORD dst_unused:UNUSED_PAD src0_sel:DWORD src1_sel:WORD_1
	v_xor_b32_sdwa v1, v4, sext(v1) dst_sel:DWORD dst_unused:UNUSED_PAD src0_sel:DWORD src1_sel:WORD_0
	v_lshlrev_b32_e32 v4, 4, v7
	v_lshlrev_b32_e32 v7, 4, v1
	v_and_b32_e32 v130, 0x70, v7
	v_lshl_add_u32 v158, v5, 3, v2
	v_and_b32_e32 v1, 0x70, v4
	v_lshl_or_b32 v132, v3, 7, v130
	v_lshlrev_b32_e32 v3, 1, v158
	v_lshrrev_b32_e32 v4, 2, v158
	v_and_b32_e32 v2, 3, v2
	v_and_b32_e32 v3, 24, v3
	v_and_b32_e32 v4, 4, v4
	v_and_or_b32 v2, v158, s0, v2
	s_add_u32 s30, s90, 0x3ba13600
	v_or3_b32 v2, v2, v4, v3
	s_addc_u32 s31, s91, 0
	v_lshl_or_b32 v134, v2, 7, v1
	s_ashr_i32 s0, s8, 6
	v_lshlrev_b32_e32 v2, 2, v131
	s_add_i32 s2, 0, 0x20000
	v_lshlrev_b32_e32 v4, 2, v158
	s_ashr_i32 s6, s8, 8
	s_lshl_b32 s34, s0, 10
	v_add_u32_e32 v3, s2, v2
	v_add_u32_e32 v5, s2, v4
	s_add_i32 s2, 0, 0x20200
	s_mul_i32 s3, s51, 0xb00000
	v_add_u32_e32 v2, s2, v2
	v_add_u32_e32 v4, s2, v4
	s_mul_hi_i32 s2, s51, 0xb00000
	s_add_u32 s4, s30, s3
	s_addc_u32 s5, s31, s2
	s_ashr_i32 s17, s16, 31
	s_lshl_b64 s[2:3], s[16:17], 19
	s_add_u32 s2, s4, s2
	s_addc_u32 s3, s5, s3
	s_add_i32 s17, s34, 0
	s_waitcnt lgkmcnt(0)
	s_barrier
	ds_read_b32 v3, v3
	ds_read_b32 v5, v5
	s_add_i32 m0, s17, 0x10000
	ds_read_b32 v2, v2
	ds_read_b32 v4, v4
	global_load_lds_dwordx4 v132, s[2:3]
	s_add_i32 m0, s17, 0x12000
	s_add_u32 s4, s2, 0x40000
	global_load_lds_dwordx4 v134, s[2:3]
	s_addc_u32 s5, s3, 0
	s_add_i32 m0, s17, 0x14000
	s_waitcnt lgkmcnt(0)
	v_lshlrev_b32_e32 v3, 11, v3
	global_load_lds_dwordx4 v132, s[4:5]
	s_add_i32 m0, s17, 0x16000
	v_lshlrev_b32_e32 v5, 11, v5
	v_or_b32_e32 v152, v3, v130
	global_load_lds_dwordx4 v134, s[4:5]
	s_mov_b32 m0, s17
	s_add_i32 s35, s17, 0x2000
	v_or_b32_e32 v153, v5, v1
	global_load_lds_dwordx4 v152, s[82:83]
	s_mov_b32 m0, s35
	s_add_i32 s36, s17, 0x4000
	v_lshl_or_b32 v148, v2, 11, v130
	global_load_lds_dwordx4 v153, s[82:83]
	s_mov_b32 m0, s36
	s_add_i32 s37, s17, 0x6000
	v_lshl_or_b32 v150, v4, 11, v1
	global_load_lds_dwordx4 v148, s[82:83]
	s_mov_b32 m0, s37
	v_mov_b32_e32 v137, 0
	global_load_lds_dwordx4 v150, s[82:83]
	s_cmp_eq_u32 s6, 1
	s_mov_b32 s38, 0
	v_mov_b32_e32 v133, v137
	v_mov_b32_e32 v135, v137
	v_mov_b32_e32 v136, v152
	v_mov_b32_e32 v2, v153
	s_cselect_b64 s[4:5], -1, 0
	s_cmp_lg_u32 s6, 1
	v_mov_b32_e32 v3, v137
	s_cbranch_scc1 .LBB0_2329
.LBB0_2329:
	s_lshl_b32 s7, s7, 3
	s_lshl_b32 s39, s6, 6
	s_lshl_b32 s6, s0, 5
	s_sub_i32 s1, s1, s7
	s_and_b32 s40, s6, 0x60
	s_add_u32 s6, s2, 0x4000
	s_addc_u32 s7, s3, 0
	s_add_i32 m0, s17, 0x18000
	v_lshl_add_u64 v[4:5], s[6:7], 0, v[132:133]
	s_waitcnt vmcnt(2)
	s_barrier
	global_load_lds_dwordx4 v[4:5], off
	s_add_i32 m0, s17, 0x1a000
	v_lshl_add_u64 v[4:5], s[6:7], 0, v[134:135]
	s_add_u32 s6, s90, 0x4213680
	s_addc_u32 s7, s91, 0
	s_add_i32 s41, s17, 0x8000
	s_add_i32 s42, s17, 0xa000
	global_load_lds_dwordx4 v[4:5], off
	v_lshl_add_u64 v[4:5], s[6:7], 0, v[136:137]
	s_mov_b32 m0, s41
	s_add_u32 s10, s2, 0x44000
	global_load_lds_dwordx4 v[4:5], off
	v_lshl_add_u64 v[2:3], s[6:7], 0, v[2:3]
	s_mov_b32 m0, s42
	s_addc_u32 s11, s3, 0
	global_load_lds_dwordx4 v[2:3], off
	s_add_i32 m0, s17, 0x1c000
	v_lshl_add_u64 v[2:3], s[10:11], 0, v[132:133]
	global_load_lds_dwordx4 v[2:3], off
	v_lshl_add_u64 v[2:3], s[10:11], 0, v[134:135]
	s_add_i32 m0, s17, 0x1e000
	v_bfe_u32 v4, v6, 4, 2
	global_load_lds_dwordx4 v[2:3], off
	v_lshrrev_b32_e32 v2, 4, v6
	v_and_b32_e32 v3, 15, v6
	v_and_b32_e32 v6, 7, v6
	v_bitop3_b32 v2, v2, v6, 3 bitop3:0x6c
	s_cmpk_lt_u32 s8, 0x100
	v_lshlrev_b32_e32 v7, 4, v2
	v_or_b32_e32 v2, s40, v3
	s_cselect_b64 s[8:9], -1, 0
	s_lshl_b32 s0, s0, 6
	v_or_b32_e32 v5, s39, v3
	v_lshlrev_b32_e32 v9, 7, v2
	v_and_or_b32 v2, s39, 64, v3
	s_and_b32 s0, s0, 64
	s_sext_i32_i8 s52, s1
	v_lshlrev_b32_e32 v5, 7, v5
	s_waitcnt vmcnt(6)
	v_lshl_or_b32 v136, v4, 4, s0
	v_readlane_b32 s0, v250, 32
	v_lshlrev_b32_e32 v2, 6, v2
	v_or_b32_e32 v8, v5, v7
	v_readlane_b32 s1, v250, 33
	v_or_b32_e32 v4, 0x800, v2
	v_or_b32_e32 v6, 0xc00, v2
	v_bitop3_b32 v3, v5, 64, v7 bitop3:0x36
	v_or_b32_e32 v159, v9, v7
	v_lshl_add_u64 v[138:139], s[0:1], 0, v[136:137]
	v_bitop3_b32 v160, v9, 64, v7 bitop3:0x36
	s_add_i32 s43, 0, 0x10000
	s_add_i32 s44, 0, 0x10800
	s_add_i32 s45, 0, 0x14000
	s_add_i32 s46, 0, 0x14800
	v_add_u32_e32 v161, 0, v8
	v_add_u32_e32 v162, 0, v3
	s_add_i32 s47, 0, 0x18800
	s_add_i32 s48, 0, 0x1c800
	s_mov_b64 s[10:11], 0x80
	v_lshlrev_b32_e32 v140, 1, v2
	v_lshlrev_b32_e32 v142, 1, v4
	v_lshlrev_b32_e32 v144, 1, v6
	v_mov_b32_e32 v163, 0xc60000
	s_barrier
	s_branch .LBB0_2332

; #define PG8_STAGE(bufoff, gbase, voff) do { _Pragma("unroll") for (int _i = 0; _i < 2; ++_i) \
;         __builtin_amdgcn_global_load_lds((const unsigned*)((const char*)(gbase) + (voff)[_i]), (LAS unsigned*)(lds + (bufoff) + ldsw + _i * 8192), 16, 0, 0); } while (0)
; #define PG8_LDA(dst, b, h) do { _Pragma("unroll") for (int m = 0; m < 4; ++m) _Pragma("unroll") for (int k = 0; k < 2; ++k) dst[m][k] = *(const LAS bf16x8*)(lds + PG8_SA(b, h) + ((aoff ^ (k * 64)) + m * 2048)); } while (0)
; #define PG8_LDB(dst, b, h) do { _Pragma("unroll") for (int n = 0; n < 2; ++n) _Pragma("unroll") for (int k = 0; k < 2; ++k) dst[n][k] = *(const LAS bf16x8*)(lds + PG8_SB(b, h) + ((boff ^ (k * 64)) + n * 2048)); } while (0)
; #define PG8_BAR __builtin_amdgcn_s_barrier()
;     ...
;             const bool last = (t == nt - 2);
;             const char* a1 = cA + (size_t)(t + 1) * kstepA;
;             const char* a2 = last ? nA : cA + (size_t)(t + 2) * kstepA; const char* b2 = last ? nB : cB + (size_t)(t + 2) * kstepB;
;             const char* a3 = a2 + kstepA; const char* b3 = b2 + kstepB;
;             unsigned vs[2][2];
;             if constexpr (GATHER) {
;                 if (last && has_next) {
; #pragma unroll
;                     for (int hh = 0; hh < 2; ++hh)
; #pragma unroll
;                         for (int i = 0; i < 2; ++i) voffN[hh][i] = (unsigned)idxl[(ui + 1) * 256 + hh * HALF + sR[i]] * (unsigned)(K * 2) + (unsigned)sC[i] * 2u;
;                 }
; #pragma unroll
;                 for (int hh = 0; hh < 2; ++hh)
; #pragma unroll
;                     for (int i = 0; i < 2; ++i) vs[hh][i] = last ? voffN[hh][i] : voffA[hh][i];
;             } else {
; #pragma unroll
;                 for (int hh = 0; hh < 2; ++hh)
; #pragma unroll
;                     for (int i = 0; i < 2; ++i) vs[hh][i] = voffA[hh][i];
;             }
;             PG8_LDB(B0, 0, 0); PG8_LDB(B1, 0, 1); PG8_SCHED; PG8_LDA(At, 0, 0); PG8_STAGE(PG8_SA(1, 1), a1, voffA[1]);
;             PG8_WAIT_V(8); PG8_WAIT_L(0); PG8_BAR; if (do0) { PG8_MMA(0, 0, At, B0); PG8_MMA(0, 1, At, B1); } PG8_BAR; PG8_SCHED;
;             PG8_LDA(At, 0, 1); PG8_STAGE(PG8_SB(0, 0), b2, voffB); PG8_STAGE(PG8_SB(0, 1), b2 + hstep, voffB); PG8_STAGE(PG8_SA(0, 0), a2, vs[0]);
;             PG8_WAIT_V(8); PG8_WAIT_L(0); PG8_BAR; if (do1) { PG8_MMA(1, 0, At, B0); PG8_MMA(1, 1, At, B1); } PG8_BAR; PG8_SCHED;
.LBB0_2337:
	v_add_u32_e32 v136, s43, v159
	v_add_u32_e32 v145, s43, v160
	ds_read_b128 v[166:169], v136
	ds_read_b128 v[170:173], v145
	v_add_u32_e32 v136, s44, v159
	s_add_u32 s22, s90, s20
	v_add_u32_e32 v145, s44, v160
	ds_read_b128 v[174:177], v136
	ds_read_b128 v[178:181], v145
	v_add_u32_e32 v136, s45, v159
	s_addc_u32 s23, s91, s21
	v_add_u32_e32 v145, s45, v160
	ds_read_b128 v[182:185], v136
	ds_read_b128 v[186:189], v145
	v_add_u32_e32 v136, s46, v159
	s_add_u32 s24, s22, 0x4213700
	v_add_u32_e32 v145, s46, v160
	ds_read_b128 v[190:193], v136
	ds_read_b128 v[194:197], v145
	s_addc_u32 s25, s23, 0
	s_and_b64 s[22:23], s[2:3], exec
	s_cselect_b32 s22, s14, s13
	s_cselect_b32 s27, s83, s25
	s_cselect_b32 s26, s82, s24
	s_cselect_b32 s23, s15, s53
	s_add_u32 s24, s22, 0x4000
	s_addc_u32 s25, s23, 0
	v_cndmask_b32_e64 v136, v152, v146, s[2:3]
	v_cndmask_b32_e64 v232, v153, v147, s[2:3]
	v_cndmask_b32_e64 v145, v148, v164, s[2:3]
	v_cndmask_b32_e64 v149, v150, v165, s[2:3]
	v_lshl_add_u64 v[234:235], v[156:157], 0, s[20:21]
	s_add_i32 m0, s17, 0xc000
	ds_read_b128 v[200:203], v161
	ds_read_b128 v[204:207], v161 offset:2048
	ds_read_b128 v[208:211], v162
	ds_read_b128 v[212:215], v162 offset:2048
	ds_read_b128 v[216:219], v161 offset:4096
	ds_read_b128 v[220:223], v161 offset:6144
	ds_read_b128 v[224:227], v162 offset:4096
	ds_read_b128 v[228:231], v162 offset:6144
	global_load_lds_dwordx4 v[234:235], off
	v_lshl_add_u64 v[234:235], v[154:155], 0, s[20:21]
	s_add_i32 m0, s17, 0xe000
	s_nop 0
	global_load_lds_dwordx4 v[234:235], off
	s_waitcnt vmcnt(8)
	s_waitcnt lgkmcnt(0)
	s_bitcmp0_b32 s4, 0
	s_cbranch_scc0 .Lsb_guL1_0
	s_barrier
.Lsb_guL1_0:
	s_setprio 1
	s_waitcnt lgkmcnt(0)
	v_mfma_f32_16x16x32_bf16 v[126:129], v[166:169], v[200:203], v[126:129]
	v_mfma_f32_16x16x32_bf16 v[122:125], v[174:177], v[200:203], v[122:125]
	v_mfma_f32_16x16x32_bf16 v[110:113], v[166:169], v[204:207], v[110:113]
	v_mfma_f32_16x16x32_bf16 v[106:109], v[174:177], v[204:207], v[106:109]
	v_mfma_f32_16x16x32_bf16 v[94:97], v[166:169], v[216:219], v[94:97]
	v_mfma_f32_16x16x32_bf16 v[90:93], v[174:177], v[216:219], v[90:93]
	v_mfma_f32_16x16x32_bf16 v[78:81], v[166:169], v[220:223], v[78:81]
	v_mfma_f32_16x16x32_bf16 v[74:77], v[174:177], v[220:223], v[74:77]
	v_mfma_f32_16x16x32_bf16 v[126:129], v[170:173], v[208:211], v[126:129]
	v_mfma_f32_16x16x32_bf16 v[122:125], v[178:181], v[208:211], v[122:125]
	v_mfma_f32_16x16x32_bf16 v[110:113], v[170:173], v[212:215], v[110:113]
	v_mfma_f32_16x16x32_bf16 v[106:109], v[178:181], v[212:215], v[106:109]
	v_mfma_f32_16x16x32_bf16 v[94:97], v[170:173], v[224:227], v[94:97]
	v_mfma_f32_16x16x32_bf16 v[90:93], v[178:181], v[224:227], v[90:93]
	v_mfma_f32_16x16x32_bf16 v[78:81], v[170:173], v[228:231], v[78:81]
	v_mfma_f32_16x16x32_bf16 v[74:77], v[178:181], v[228:231], v[74:77]
	s_setprio 0
	s_setprio 1
	v_mfma_f32_16x16x32_bf16 v[118:121], v[182:185], v[200:203], v[118:121]
	v_mfma_f32_16x16x32_bf16 v[114:117], v[190:193], v[200:203], v[114:117]
	v_mfma_f32_16x16x32_bf16 v[102:105], v[182:185], v[204:207], v[102:105]
	v_mfma_f32_16x16x32_bf16 v[98:101], v[190:193], v[204:207], v[98:101]
	v_mfma_f32_16x16x32_bf16 v[86:89], v[182:185], v[216:219], v[86:89]
	v_mfma_f32_16x16x32_bf16 v[82:85], v[190:193], v[216:219], v[82:85]
	v_mfma_f32_16x16x32_bf16 v[70:73], v[182:185], v[220:223], v[70:73]
	v_mfma_f32_16x16x32_bf16 v[66:69], v[190:193], v[220:223], v[66:69]
	v_mfma_f32_16x16x32_bf16 v[118:121], v[186:189], v[208:211], v[118:121]
	v_mfma_f32_16x16x32_bf16 v[114:117], v[194:197], v[208:211], v[114:117]
	v_mfma_f32_16x16x32_bf16 v[102:105], v[186:189], v[212:215], v[102:105]
	v_mfma_f32_16x16x32_bf16 v[98:101], v[194:197], v[212:215], v[98:101]
	v_mfma_f32_16x16x32_bf16 v[86:89], v[186:189], v[224:227], v[86:89]
	v_mfma_f32_16x16x32_bf16 v[82:85], v[194:197], v[224:227], v[82:85]
	v_mfma_f32_16x16x32_bf16 v[70:73], v[186:189], v[228:231], v[70:73]
	v_mfma_f32_16x16x32_bf16 v[66:69], v[194:197], v[228:231], v[66:69]
	s_setprio 0
	s_bitcmp1_b32 s4, 0
	s_cbranch_scc0 .Lsb_guL1_1
	s_barrier
; #define PG8_STAGE(bufoff, gbase, voff) do { _Pragma("unroll") for (int _i = 0; _i < 2; ++_i) \
;         __builtin_amdgcn_global_load_lds((const unsigned*)((const char*)(gbase) + (voff)[_i]), (LAS unsigned*)(lds + (bufoff) + ldsw + _i * 8192), 16, 0, 0); } while (0)
; #define PG8_LDA(dst, b, h) do { _Pragma("unroll") for (int m = 0; m < 4; ++m) _Pragma("unroll") for (int k = 0; k < 2; ++k) dst[m][k] = *(const LAS bf16x8*)(lds + PG8_SA(b, h) + ((aoff ^ (k * 64)) + m * 2048)); } while (0)
; #define PG8_LDB(dst, b, h) do { _Pragma("unroll") for (int n = 0; n < 2; ++n) _Pragma("unroll") for (int k = 0; k < 2; ++k) dst[n][k] = *(const LAS bf16x8*)(lds + PG8_SB(b, h) + ((boff ^ (k * 64)) + n * 2048)); } while (0)
; #define PG8_MMA(ai, bj, At, Bt) do { __builtin_amdgcn_s_setprio(1); _Pragma("unroll") for (int m = 0; m < 4; ++m) _Pragma("unroll") for (int n = 0; n < 2; ++n) _Pragma("unroll") for (int k = 0; k < 2; ++k) \
;         acc[ai][bj][m][n] = __builtin_amdgcn_mfma_f32_16x16x32_bf16(Bt[n][k], At[m][k], acc[ai][bj][m][n], 0, 0, 0); __builtin_amdgcn_s_setprio(0); } while (0)
; #define PG8_WAIT_V(n) asm volatile("s_waitcnt vmcnt(" #n ")" ::: "memory")
; #define PG8_WAIT_L(n) asm volatile("s_waitcnt lgkmcnt(" #n ")" ::: "memory")
; #define PG8_BAR __builtin_amdgcn_s_barrier()
; #define PG8_SCHED __builtin_amdgcn_sched_barrier(0)
;     ...
;             PG8_LDA(At, 0, 1); PG8_STAGE(PG8_SB(0, 0), b2, voffB); PG8_STAGE(PG8_SB(0, 1), b2 + hstep, voffB); PG8_STAGE(PG8_SA(0, 0), a2, vs[0]);
;             PG8_WAIT_V(8); PG8_WAIT_L(0); PG8_BAR; if (do1) { PG8_MMA(1, 0, At, B0); PG8_MMA(1, 1, At, B1); } PG8_BAR; PG8_SCHED;
;             PG8_LDB(B0, 1, 0); PG8_LDB(B1, 1, 1); PG8_SCHED; PG8_LDA(At, 1, 0); PG8_STAGE(PG8_SA(0, 1), a2, vs[1]);
;             PG8_WAIT_V(8); PG8_WAIT_L(0); PG8_BAR; if (do0) { PG8_MMA(0, 0, At, B0); PG8_MMA(0, 1, At, B1); } PG8_BAR; PG8_SCHED;
.Lsb_guL1_1:
	s_add_i32 s2, s43, s34
	v_lshl_add_u64 v[234:235], s[22:23], 0, v[132:133]
	s_mov_b32 m0, s2
	ds_read_b128 v[200:203], v161 offset:16384
	ds_read_b128 v[204:207], v161 offset:18432
	ds_read_b128 v[208:211], v162 offset:16384
	ds_read_b128 v[212:215], v162 offset:18432
	ds_read_b128 v[216:219], v161 offset:20480
	ds_read_b128 v[220:223], v161 offset:22528
	ds_read_b128 v[224:227], v162 offset:20480
	ds_read_b128 v[228:231], v162 offset:22528
	global_load_lds_dwordx4 v[234:235], off
	s_add_i32 m0, s2, 0x2000
	s_add_u32 s2, s22, 0x40000
	v_lshl_add_u64 v[234:235], s[22:23], 0, v[134:135]
	s_addc_u32 s3, s23, 0
	s_add_i32 s55, s45, s34
	global_load_lds_dwordx4 v[234:235], off
	v_lshl_add_u64 v[234:235], s[2:3], 0, v[132:133]
	s_mov_b32 m0, s55
	v_mov_b32_e32 v233, v137
	global_load_lds_dwordx4 v[234:235], off
	v_lshl_add_u64 v[234:235], s[2:3], 0, v[134:135]
	s_add_i32 m0, s55, 0x2000
	s_nop 0
	global_load_lds_dwordx4 v[234:235], off
	s_mov_b32 m0, s17
	v_lshl_add_u64 v[234:235], s[26:27], 0, v[136:137]
	global_load_lds_dwordx4 v136, s[26:27]
	s_mov_b32 m0, s35
	s_nop 0
	global_load_lds_dwordx4 v232, s[26:27]
	s_waitcnt vmcnt(8)
	s_waitcnt lgkmcnt(0)
	v_lshl_add_u64 v[232:233], s[26:27], 0, v[232:233]
	s_bitcmp0_b32 s4, 0
	s_cbranch_scc0 .Lsb_guL1_2
	s_barrier
.Lsb_guL1_2:
	s_setprio 1
	s_waitcnt lgkmcnt(0)
	v_mfma_f32_16x16x32_bf16 v[62:65], v[166:169], v[200:203], v[62:65]
	v_mfma_f32_16x16x32_bf16 v[58:61], v[174:177], v[200:203], v[58:61]
	v_mfma_f32_16x16x32_bf16 v[46:49], v[166:169], v[204:207], v[46:49]
	v_mfma_f32_16x16x32_bf16 v[42:45], v[174:177], v[204:207], v[42:45]
	v_mfma_f32_16x16x32_bf16 v[30:33], v[166:169], v[216:219], v[30:33]
	v_mfma_f32_16x16x32_bf16 v[26:29], v[174:177], v[216:219], v[26:29]
	v_mfma_f32_16x16x32_bf16 v[14:17], v[166:169], v[220:223], v[14:17]
	v_mfma_f32_16x16x32_bf16 v[10:13], v[174:177], v[220:223], v[10:13]
	v_mfma_f32_16x16x32_bf16 v[62:65], v[170:173], v[208:211], v[62:65]
	v_mfma_f32_16x16x32_bf16 v[58:61], v[178:181], v[208:211], v[58:61]
	v_mfma_f32_16x16x32_bf16 v[46:49], v[170:173], v[212:215], v[46:49]
	v_mfma_f32_16x16x32_bf16 v[42:45], v[178:181], v[212:215], v[42:45]
	v_mfma_f32_16x16x32_bf16 v[30:33], v[170:173], v[224:227], v[30:33]
	v_mfma_f32_16x16x32_bf16 v[26:29], v[178:181], v[224:227], v[26:29]
	v_mfma_f32_16x16x32_bf16 v[14:17], v[170:173], v[228:231], v[14:17]
	v_mfma_f32_16x16x32_bf16 v[10:13], v[178:181], v[228:231], v[10:13]
	s_setprio 0
	s_setprio 1
	v_mfma_f32_16x16x32_bf16 v[54:57], v[182:185], v[200:203], v[54:57]
	v_mfma_f32_16x16x32_bf16 v[50:53], v[190:193], v[200:203], v[50:53]
	v_mfma_f32_16x16x32_bf16 v[38:41], v[182:185], v[204:207], v[38:41]
	v_mfma_f32_16x16x32_bf16 v[34:37], v[190:193], v[204:207], v[34:37]
	v_mfma_f32_16x16x32_bf16 v[22:25], v[182:185], v[216:219], v[22:25]
	v_mfma_f32_16x16x32_bf16 v[18:21], v[190:193], v[216:219], v[18:21]
	v_mfma_f32_16x16x32_bf16 v[6:9], v[182:185], v[220:223], v[6:9]
	v_mfma_f32_16x16x32_bf16 v[2:5], v[190:193], v[220:223], v[2:5]
	v_mfma_f32_16x16x32_bf16 v[54:57], v[186:189], v[208:211], v[54:57]
	v_mfma_f32_16x16x32_bf16 v[50:53], v[194:197], v[208:211], v[50:53]
	v_mfma_f32_16x16x32_bf16 v[38:41], v[186:189], v[212:215], v[38:41]
	v_mfma_f32_16x16x32_bf16 v[34:37], v[194:197], v[212:215], v[34:37]
	v_mfma_f32_16x16x32_bf16 v[22:25], v[186:189], v[224:227], v[22:25]
	v_mfma_f32_16x16x32_bf16 v[18:21], v[194:197], v[224:227], v[18:21]
	v_mfma_f32_16x16x32_bf16 v[6:9], v[186:189], v[228:231], v[6:9]
	v_mfma_f32_16x16x32_bf16 v[2:5], v[194:197], v[228:231], v[2:5]
	s_setprio 0
	s_bitcmp1_b32 s4, 0
	s_cbranch_scc0 .Lsb_guL1_3
	s_barrier
.Lsb_guL1_3:
	s_add_i32 s2, 0, 0x18000
	v_add_u32_e32 v136, s2, v159
	v_add_u32_e32 v151, s2, v160
	ds_read_b128 v[166:169], v136
	ds_read_b128 v[170:173], v151
	v_add_u32_e32 v136, s47, v159
	s_add_i32 s55, 0, 0x1c000
	v_add_u32_e32 v151, s47, v160
	ds_read_b128 v[174:177], v136
	ds_read_b128 v[178:181], v151
	v_add_u32_e32 v136, s55, v159
	v_add_u32_e32 v151, s55, v160
	ds_read_b128 v[182:185], v136
	ds_read_b128 v[186:189], v151
	v_add_u32_e32 v136, s48, v159
	v_add_u32_e32 v151, s48, v160
	ds_read_b128 v[190:193], v136
	ds_read_b128 v[194:197], v151
	s_mov_b32 m0, s36
	ds_read_b128 v[200:203], v161 offset:32768
	ds_read_b128 v[204:207], v161 offset:34816
	ds_read_b128 v[208:211], v162 offset:32768
	ds_read_b128 v[212:215], v162 offset:34816
	ds_read_b128 v[216:219], v161 offset:36864
	ds_read_b128 v[220:223], v161 offset:38912
	ds_read_b128 v[224:227], v162 offset:36864
	ds_read_b128 v[228:231], v162 offset:38912
	global_load_lds_dwordx4 v145, s[26:27]
	s_mov_b32 m0, s37
	s_nop 0
	global_load_lds_dwordx4 v149, s[26:27]
	s_waitcnt vmcnt(8)
	s_waitcnt lgkmcnt(0)
	s_bitcmp0_b32 s4, 0
	s_cbranch_scc0 .Lsb_guL1_4
	s_barrier

; #define PG8_STAGE(bufoff, gbase, voff) do { _Pragma("unroll") for (int _i = 0; _i < 2; ++_i) \
;         __builtin_amdgcn_global_load_lds((const unsigned*)((const char*)(gbase) + (voff)[_i]), (LAS unsigned*)(lds + (bufoff) + ldsw + _i * 8192), 16, 0, 0); } while (0)
; #define PG8_LDA(dst, b, h) do { _Pragma("unroll") for (int m = 0; m < 4; ++m) _Pragma("unroll") for (int k = 0; k < 2; ++k) dst[m][k] = *(const LAS bf16x8*)(lds + PG8_SA(b, h) + ((aoff ^ (k * 64)) + m * 2048)); } while (0)
; #define PG8_MMA(ai, bj, At, Bt) do { __builtin_amdgcn_s_setprio(1); _Pragma("unroll") for (int m = 0; m < 4; ++m) _Pragma("unroll") for (int n = 0; n < 2; ++n) _Pragma("unroll") for (int k = 0; k < 2; ++k) \
;         acc[ai][bj][m][n] = __builtin_amdgcn_mfma_f32_16x16x32_bf16(Bt[n][k], At[m][k], acc[ai][bj][m][n], 0, 0, 0); __builtin_amdgcn_s_setprio(0); } while (0)
; #define PG8_WAIT_V(n) asm volatile("s_waitcnt vmcnt(" #n ")" ::: "memory")
; #define PG8_WAIT_L(n) asm volatile("s_waitcnt lgkmcnt(" #n ")" ::: "memory")
; #define PG8_BAR __builtin_amdgcn_s_barrier()
; #define PG8_SCHED __builtin_amdgcn_sched_barrier(0)
;     ...
;             PG8_LDA(At, 1, 1); PG8_STAGE(PG8_SB(1, 0), b3, voffB); PG8_STAGE(PG8_SB(1, 1), b3 + hstep, voffB); PG8_STAGE(PG8_SA(1, 0), a3, vs[0]);
;             PG8_WAIT_V(8); PG8_WAIT_L(0); PG8_BAR; if (do1) { PG8_MMA(1, 0, At, B0); PG8_MMA(1, 1, At, B1); } PG8_BAR; PG8_SCHED;
.Lsb_guL1_5:
	s_add_i32 s2, s2, s34
	v_lshl_add_u64 v[236:237], s[24:25], 0, v[132:133]
	s_mov_b32 m0, s2
	ds_read_b128 v[200:203], v161 offset:49152
	ds_read_b128 v[204:207], v161 offset:51200
	ds_read_b128 v[208:211], v162 offset:49152
	ds_read_b128 v[212:215], v162 offset:51200
	ds_read_b128 v[216:219], v161 offset:53248
	ds_read_b128 v[220:223], v161 offset:55296
	ds_read_b128 v[224:227], v162 offset:53248
	ds_read_b128 v[228:231], v162 offset:55296
	global_load_lds_dwordx4 v[236:237], off
	s_add_i32 m0, s2, 0x2000
	s_add_u32 s2, s22, 0x44000
	v_lshl_add_u64 v[236:237], s[24:25], 0, v[134:135]
	s_addc_u32 s3, s23, 0
	s_add_i32 s22, s55, s34
	global_load_lds_dwordx4 v[236:237], off
	v_lshl_add_u64 v[236:237], s[2:3], 0, v[132:133]
	s_mov_b32 m0, s22
	v_lshl_add_u64 v[234:235], v[234:235], 0, s[10:11]
	global_load_lds_dwordx4 v[236:237], off
	v_lshl_add_u64 v[236:237], s[2:3], 0, v[134:135]
	s_add_i32 m0, s22, 0x2000
	v_lshl_add_u64 v[232:233], v[232:233], 0, s[10:11]
	global_load_lds_dwordx4 v[236:237], off
	s_mov_b32 m0, s41
	s_nop 0
	global_load_lds_dwordx4 v[234:235], off
	s_mov_b32 m0, s42
	s_nop 0
	global_load_lds_dwordx4 v[232:233], off
	s_waitcnt vmcnt(8)
	s_waitcnt lgkmcnt(0)
	s_bitcmp0_b32 s4, 0
	s_cbranch_scc0 .Lsb_guL1_6
	s_barrier

; #define PG8_WAIT_V(n) asm volatile("s_waitcnt vmcnt(" #n ")" ::: "memory")
; #define PG8_WAIT_L(n) asm volatile("s_waitcnt lgkmcnt(" #n ")" ::: "memory")
;     ...
;         for (int t = 0; t < nt; t += 2) {
;             const bool last = (t == nt - 2);
;             const char* a1 = cA + (size_t)(t + 1) * kstepA;
;             const char* a2 = last ? nA : cA + (size_t)(t + 2) * kstepA; const char* b2 = last ? nB : cB + (size_t)(t + 2) * kstepB;
;             const char* a3 = a2 + kstepA; const char* b3 = b2 + kstepB;
;             unsigned vs[2][2];
;             if constexpr (GATHER) {
;                 if (last && has_next) {
; #pragma unroll
;                     for (int hh = 0; hh < 2; ++hh)
; #pragma unroll
;                         for (int i = 0; i < 2; ++i) voffN[hh][i] = (unsigned)idxl[(ui + 1) * 256 + hh * HALF + sR[i]] * (unsigned)(K * 2) + (unsigned)sC[i] * 2u;
;                 }
; #pragma unroll
;                 for (int hh = 0; hh < 2; ++hh)
; #pragma unroll
;                     for (int i = 0; i < 2; ++i) vs[hh][i] = last ? voffN[hh][i] : voffA[hh][i];
;             } else {
; #pragma unroll
;                 for (int hh = 0; hh < 2; ++hh)
; #pragma unroll
;                     for (int i = 0; i < 2; ++i) vs[hh][i] = voffA[hh][i];
;             }
;             PG8_LDB(B0, 0, 0); PG8_LDB(B1, 0, 1); PG8_SCHED; PG8_LDA(At, 0, 0); PG8_STAGE(PG8_SA(1, 1), a1, voffA[1]);
;             PG8_WAIT_V(8); PG8_WAIT_L(0); PG8_BAR; if (do0) { PG8_MMA(0, 0, At, B0); PG8_MMA(0, 1, At, B1); } PG8_BAR; PG8_SCHED;
;             PG8_LDA(At, 0, 1); PG8_STAGE(PG8_SB(0, 0), b2, voffB); PG8_STAGE(PG8_SB(0, 1), b2 + hstep, voffB); PG8_STAGE(PG8_SA(0, 0), a2, vs[0]);
;             PG8_WAIT_V(8); PG8_WAIT_L(0); PG8_BAR; if (do1) { PG8_MMA(1, 0, At, B0); PG8_MMA(1, 1, At, B1); } PG8_BAR; PG8_SCHED;
;             PG8_LDB(B0, 1, 0); PG8_LDB(B1, 1, 1); PG8_SCHED; PG8_LDA(At, 1, 0); PG8_STAGE(PG8_SA(0, 1), a2, vs[1]);
;             PG8_WAIT_V(8); PG8_WAIT_L(0); PG8_BAR; if (do0) { PG8_MMA(0, 0, At, B0); PG8_MMA(0, 1, At, B1); } PG8_BAR; PG8_SCHED;
;             PG8_LDA(At, 1, 1); PG8_STAGE(PG8_SB(1, 0), b3, voffB); PG8_STAGE(PG8_SB(1, 1), b3 + hstep, voffB); PG8_STAGE(PG8_SA(1, 0), a3, vs[0]);
;             PG8_WAIT_V(8); PG8_WAIT_L(0); PG8_BAR; if (do1) { PG8_MMA(1, 0, At, B0); PG8_MMA(1, 1, At, B1); } PG8_BAR; PG8_SCHED;
;         }
.Lsb_guL1_7:
	s_add_i32 s54, s54, 2
	s_add_u32 s13, s13, 0x8000
	s_addc_u32 s53, s53, 0
	s_add_u32 s20, s20, 0x100
	s_addc_u32 s21, s21, 0
	s_cmp_gt_u32 s54, 13
	s_cbranch_scc1 .LBB0_2340

; __device__ __forceinline__ float silu_fast(float v) { return v * __builtin_amdgcn_rcpf(1.f + __builtin_amdgcn_exp2f(-1.4426950408889634f * v)); }
; __device__ __forceinline__ u32x4 pack8(const f32x4 a, const f32x4 b) { u32x4 w; w.x = cvt_pk_bf16(a[0], a[1]); w.y = cvt_pk_bf16(a[2], a[3]); w.z = cvt_pk_bf16(b[0], b[1]); w.w = cvt_pk_bf16(b[2], b[3]); return w; }
; #define PG8_BAR __builtin_amdgcn_s_barrier()
;     __device__ __forceinline__ void operator()(const f32x4 (&acc)[2][2][4][2], const Unit& u, int wr, int wc, int fr, int fq) const {
;         const int row0 = u.pm * BM + wr * 64 + fr, col0 = u.pn * HALF + wc * 32 + 8 * fq;
;         bf16_t* base = HID + (size_t)u.z * MEXP * FF;
; #pragma unroll
;         for (int ai = 0; ai < 2; ++ai)
; #pragma unroll
;             for (int m = 0; m < 4; ++m) { f32x4 h[2];
; #pragma unroll
;                 for (int n = 0; n < 2; ++n)
; #pragma unroll
;                     for (int j = 0; j < 4; ++j) h[n][j] = silu_fast(acc[ai][0][m][n][j]) * acc[ai][1][m][n][j];
;                 const int row = row0 + ai * HALF + m * 16;
;                 *(u32x4*)(base + ((size_t)(row >> 7) * (FF / 64) + (col0 >> 6)) * 8192 + (row & 127) * 64 + (col0 & 63)) = pack8(h[0], h[1]); }
;     ...
;         if (wr == 0) PG8_BAR;
.LBB0_2342:
	v_mul_f32_e32 v136, 0xbfb8aa3b, v126
	v_exp_f32_e32 v136, v136
	v_mul_f32_e32 v141, 0xbfb8aa3b, v127
	v_exp_f32_e32 v141, v141
	s_lshl_b32 s13, s52, 8
	v_add_f32_e32 v136, 1.0, v136
	v_rcp_f32_e32 v152, v136
	v_add_f32_e32 v136, 1.0, v141
	v_rcp_f32_e32 v153, v136
	v_mul_f32_e32 v136, 0xbfb8aa3b, v128
	v_mul_f32_e32 v141, 0xbfb8aa3b, v129
	v_exp_f32_e32 v136, v136
	v_exp_f32_e32 v141, v141
	v_pk_mul_f32 v[126:127], v[126:127], v[152:153]
	s_add_i32 s13, s13, s39
	v_pk_mul_f32 v[118:119], v[126:127], v[118:119]
	v_add_f32_e32 v126, 1.0, v136
	v_add_f32_e32 v127, 1.0, v141
	v_mul_f32_e32 v136, 0xbfb8aa3b, v122
	v_rcp_f32_e32 v126, v126
	v_rcp_f32_e32 v127, v127
	v_exp_f32_e32 v136, v136
	v_mul_f32_e32 v141, 0xbfb8aa3b, v123
	v_exp_f32_e32 v141, v141
	v_pk_mul_f32 v[126:127], v[128:129], v[126:127]
	v_add_f32_e32 v128, 1.0, v136
	v_mul_f32_e32 v136, 0xbfb8aa3b, v124
	v_add_f32_e32 v129, 1.0, v141
	v_exp_f32_e32 v136, v136
	v_mul_f32_e32 v141, 0xbfb8aa3b, v125
	v_exp_f32_e32 v141, v141
	v_rcp_f32_e32 v128, v128
	v_add_f32_e32 v136, 1.0, v136
	v_rcp_f32_e32 v129, v129
	v_rcp_f32_e32 v152, v136
	v_add_f32_e32 v136, 1.0, v141
	v_rcp_f32_e32 v153, v136
	s_lshl_b32 s2, s16, 7
	v_pk_mul_f32 v[122:123], v[122:123], v[128:129]
	s_or_b32 s2, s2, s40
	s_ashr_i32 s16, s13, 7
	v_pk_mul_f32 v[122:123], v[122:123], v[114:115]
	v_pk_mul_f32 v[114:115], v[124:125], v[152:153]
	s_ashr_i32 s3, s2, 6
	v_mad_i64_i32 v[148:149], s[18:19], s51, v163, v[138:139]
	s_mul_i32 s16, s16, 44
	v_pk_mul_f32 v[124:125], v[114:115], v[116:117]
	v_mul_f32_e32 v117, 0xbfb8aa3b, v110
	s_ashr_i32 s2, s3, 31
	s_ashr_i32 s19, s16, 31
	v_cvt_pk_bf16_f32 v114, v118, v119
	v_exp_f32_e32 v118, v117
	v_mul_f32_e32 v117, 0xbfb8aa3b, v111
	s_add_u32 s18, s16, s3
	v_exp_f32_e32 v119, v117
	s_addc_u32 s19, s19, s2
	s_lshl_b64 s[18:19], s[18:19], 14
	v_lshl_add_u64 v[150:151], v[148:149], 0, s[18:19]
	v_pk_mul_f32 v[120:121], v[126:127], v[120:121]
	v_mov_b32_e32 v141, v137
	v_cvt_pk_bf16_f32 v115, v120, v121
	v_cvt_pk_bf16_f32 v116, v122, v123
	v_cvt_pk_bf16_f32 v117, v124, v125
	v_add_f32_e32 v118, 1.0, v118
	v_add_f32_e32 v119, 1.0, v119
	v_lshl_add_u64 v[120:121], v[150:151], 0, v[140:141]
	v_rcp_f32_e32 v118, v118
	v_rcp_f32_e32 v119, v119
	global_store_dwordx4 v[120:121], v[114:117], off
	v_mov_b32_e32 v143, v137
	v_mov_b32_e32 v145, v137
	v_mul_f32_e32 v114, 0xbfb8aa3b, v112
	v_mul_f32_e32 v115, 0xbfb8aa3b, v113
	v_exp_f32_e32 v114, v114
	v_exp_f32_e32 v115, v115
	v_pk_mul_f32 v[110:111], v[110:111], v[118:119]
	s_addk_i32 s13, 0x80
	v_pk_mul_f32 v[102:103], v[110:111], v[102:103]
	v_add_f32_e32 v110, 1.0, v114
	v_add_f32_e32 v111, 1.0, v115
	v_mul_f32_e32 v114, 0xbfb8aa3b, v106
	v_mul_f32_e32 v115, 0xbfb8aa3b, v107
	v_rcp_f32_e32 v110, v110
	v_rcp_f32_e32 v111, v111
	v_exp_f32_e32 v114, v114
	v_exp_f32_e32 v115, v115
	s_ashr_i32 s13, s13, 7
	v_pk_mul_f32 v[110:111], v[112:113], v[110:111]
	v_add_f32_e32 v112, 1.0, v114
	v_add_f32_e32 v113, 1.0, v115
	v_mul_f32_e32 v114, 0xbfb8aa3b, v108
	v_mul_f32_e32 v115, 0xbfb8aa3b, v109
	v_exp_f32_e32 v114, v114
	v_exp_f32_e32 v115, v115
	v_rcp_f32_e32 v112, v112
	v_rcp_f32_e32 v113, v113
	v_add_f32_e32 v114, 1.0, v114
	v_add_f32_e32 v115, 1.0, v115
	v_rcp_f32_e32 v114, v114
	v_rcp_f32_e32 v115, v115
	v_pk_mul_f32 v[106:107], v[106:107], v[112:113]
	v_pk_mul_f32 v[104:105], v[110:111], v[104:105]
	v_pk_mul_f32 v[106:107], v[106:107], v[98:99]
	v_pk_mul_f32 v[98:99], v[108:109], v[114:115]
	s_mul_i32 s13, s13, 44
	v_pk_mul_f32 v[108:109], v[98:99], v[100:101]
	v_mul_f32_e32 v99, 0xbfb8aa3b, v94
	v_exp_f32_e32 v100, v99
	v_mul_f32_e32 v99, 0xbfb8aa3b, v95
	v_exp_f32_e32 v101, v99
	v_cvt_pk_bf16_f32 v98, v102, v103
	v_add_f32_e32 v100, 1.0, v100
	v_rcp_f32_e32 v102, v100
	v_add_f32_e32 v100, 1.0, v101
	v_cvt_pk_bf16_f32 v99, v104, v105
	v_rcp_f32_e32 v103, v100
	v_cvt_pk_bf16_f32 v100, v106, v107
	v_cvt_pk_bf16_f32 v101, v108, v109
	global_store_dwordx4 v[120:121], v[98:101], off offset:2048
	v_pk_mul_f32 v[94:95], v[94:95], v[102:103]
	s_ashr_i32 s16, s13, 31
	v_mul_f32_e32 v98, 0xbfb8aa3b, v96
	v_mul_f32_e32 v99, 0xbfb8aa3b, v97
	v_exp_f32_e32 v98, v98
	v_exp_f32_e32 v99, v99
	v_pk_mul_f32 v[86:87], v[94:95], v[86:87]
	s_add_u32 s18, s13, s3
	v_add_f32_e32 v94, 1.0, v98
	v_add_f32_e32 v95, 1.0, v99
	v_mul_f32_e32 v98, 0xbfb8aa3b, v90
	v_mul_f32_e32 v99, 0xbfb8aa3b, v91
	v_rcp_f32_e32 v94, v94
	v_rcp_f32_e32 v95, v95
	v_exp_f32_e32 v98, v98
	v_exp_f32_e32 v99, v99
	s_addc_u32 s19, s16, s2
	v_pk_mul_f32 v[94:95], v[96:97], v[94:95]
	v_add_f32_e32 v96, 1.0, v98
	v_add_f32_e32 v97, 1.0, v99
	v_mul_f32_e32 v98, 0xbfb8aa3b, v92
	v_mul_f32_e32 v99, 0xbfb8aa3b, v93
	v_exp_f32_e32 v98, v98
	v_exp_f32_e32 v99, v99
	v_rcp_f32_e32 v96, v96
	v_rcp_f32_e32 v97, v97
	v_add_f32_e32 v98, 1.0, v98
	v_add_f32_e32 v99, 1.0, v99
	v_rcp_f32_e32 v98, v98
	v_rcp_f32_e32 v99, v99
	v_pk_mul_f32 v[90:91], v[90:91], v[96:97]
	v_pk_mul_f32 v[88:89], v[94:95], v[88:89]
	v_pk_mul_f32 v[90:91], v[90:91], v[82:83]
	v_pk_mul_f32 v[82:83], v[92:93], v[98:99]
	s_lshl_b64 s[2:3], s[18:19], 14
	v_pk_mul_f32 v[92:93], v[82:83], v[84:85]
	v_mul_f32_e32 v85, 0xbfb8aa3b, v78
	v_cvt_pk_bf16_f32 v82, v86, v87
	v_exp_f32_e32 v86, v85
	v_mul_f32_e32 v85, 0xbfb8aa3b, v79
	v_exp_f32_e32 v87, v85
	v_cvt_pk_bf16_f32 v83, v88, v89
	v_cvt_pk_bf16_f32 v84, v90, v91
	v_cvt_pk_bf16_f32 v85, v92, v93
	v_add_f32_e32 v86, 1.0, v86
	v_add_f32_e32 v87, 1.0, v87
	v_lshl_add_u64 v[88:89], v[150:151], 0, v[142:143]
	v_rcp_f32_e32 v86, v86
	v_rcp_f32_e32 v87, v87
	global_store_dwordx4 v[88:89], v[82:85], off
	s_and_b64 vcc, exec, s[0:1]
	s_mov_b64 s[0:1], -1
	v_mul_f32_e32 v82, 0xbfb8aa3b, v80
; __device__ __forceinline__ float silu_fast(float v) { return v * __builtin_amdgcn_rcpf(1.f + __builtin_amdgcn_exp2f(-1.4426950408889634f * v)); }
; __device__ __forceinline__ u32x4 pack8(const f32x4 a, const f32x4 b) { u32x4 w; w.x = cvt_pk_bf16(a[0], a[1]); w.y = cvt_pk_bf16(a[2], a[3]); w.z = cvt_pk_bf16(b[0], b[1]); w.w = cvt_pk_bf16(b[2], b[3]); return w; }
;     __device__ __forceinline__ void operator()(const f32x4 (&acc)[2][2][4][2], const Unit& u, int wr, int wc, int fr, int fq) const {
;     ...
;             for (int m = 0; m < 4; ++m) { f32x4 h[2];
; #pragma unroll
;                 for (int n = 0; n < 2; ++n)
; #pragma unroll
;                     for (int j = 0; j < 4; ++j) h[n][j] = silu_fast(acc[ai][0][m][n][j]) * acc[ai][1][m][n][j];
;                 const int row = row0 + ai * HALF + m * 16;
;                 *(u32x4*)(base + ((size_t)(row >> 7) * (FF / 64) + (col0 >> 6)) * 8192 + (row & 127) * 64 + (col0 & 63)) = pack8(h[0], h[1]); }
	v_mul_f32_e32 v83, 0xbfb8aa3b, v81
	v_exp_f32_e32 v82, v82
	v_exp_f32_e32 v83, v83
	v_pk_mul_f32 v[78:79], v[78:79], v[86:87]
	s_nop 0
	v_pk_mul_f32 v[70:71], v[78:79], v[70:71]
	v_add_f32_e32 v78, 1.0, v82
	v_add_f32_e32 v79, 1.0, v83
	v_mul_f32_e32 v82, 0xbfb8aa3b, v74
	v_mul_f32_e32 v83, 0xbfb8aa3b, v75
	v_rcp_f32_e32 v78, v78
	v_rcp_f32_e32 v79, v79
	v_exp_f32_e32 v82, v82
	v_exp_f32_e32 v83, v83
	v_pk_mul_f32 v[78:79], v[80:81], v[78:79]
	v_add_f32_e32 v80, 1.0, v82
	v_add_f32_e32 v81, 1.0, v83
	v_mul_f32_e32 v82, 0xbfb8aa3b, v76
	v_mul_f32_e32 v83, 0xbfb8aa3b, v77
	v_exp_f32_e32 v82, v82
	v_exp_f32_e32 v83, v83
	v_rcp_f32_e32 v80, v80
	v_rcp_f32_e32 v81, v81
	v_add_f32_e32 v82, 1.0, v82
	v_add_f32_e32 v83, 1.0, v83
	v_rcp_f32_e32 v82, v82
	v_rcp_f32_e32 v83, v83
	v_pk_mul_f32 v[74:75], v[74:75], v[80:81]
	v_pk_mul_f32 v[72:73], v[78:79], v[72:73]
	v_pk_mul_f32 v[74:75], v[74:75], v[66:67]
	v_pk_mul_f32 v[66:67], v[76:77], v[82:83]
	s_nop 0
	v_pk_mul_f32 v[76:77], v[66:67], v[68:69]
	v_cvt_pk_bf16_f32 v66, v70, v71
	v_cvt_pk_bf16_f32 v67, v72, v73
	v_cvt_pk_bf16_f32 v68, v74, v75
	v_cvt_pk_bf16_f32 v69, v76, v77
	v_lshl_add_u64 v[70:71], v[150:151], 0, v[144:145]
	global_store_dwordx4 v[70:71], v[66:69], off
	s_nop 1
	v_mul_f32_e32 v66, 0xbfb8aa3b, v62
	v_exp_f32_e32 v66, v66
	v_mul_f32_e32 v67, 0xbfb8aa3b, v63
	v_exp_f32_e32 v67, v67
	v_add_f32_e32 v66, 1.0, v66
	v_rcp_f32_e32 v68, v66
	v_add_f32_e32 v66, 1.0, v67
	v_rcp_f32_e32 v69, v66
	v_lshl_add_u64 v[66:67], v[148:149], 0, s[2:3]
	v_pk_mul_f32 v[62:63], v[62:63], v[68:69]
	v_mul_f32_e32 v68, 0xbfb8aa3b, v64
	v_mul_f32_e32 v69, 0xbfb8aa3b, v65
	v_exp_f32_e32 v68, v68
	v_exp_f32_e32 v69, v69
	v_pk_mul_f32 v[54:55], v[62:63], v[54:55]
	v_add_f32_e32 v62, 1.0, v68
	v_add_f32_e32 v63, 1.0, v69
	v_mul_f32_e32 v68, 0xbfb8aa3b, v58
	v_mul_f32_e32 v69, 0xbfb8aa3b, v59
	v_rcp_f32_e32 v62, v62
	v_rcp_f32_e32 v63, v63
	v_exp_f32_e32 v68, v68
	v_exp_f32_e32 v69, v69
	v_pk_mul_f32 v[62:63], v[64:65], v[62:63]
	v_add_f32_e32 v64, 1.0, v68
	v_add_f32_e32 v65, 1.0, v69
	v_mul_f32_e32 v68, 0xbfb8aa3b, v60
	v_mul_f32_e32 v69, 0xbfb8aa3b, v61
	v_exp_f32_e32 v68, v68
	v_exp_f32_e32 v69, v69
	v_rcp_f32_e32 v64, v64
	v_rcp_f32_e32 v65, v65
	v_add_f32_e32 v68, 1.0, v68
	v_add_f32_e32 v69, 1.0, v69
	v_rcp_f32_e32 v68, v68
	v_rcp_f32_e32 v69, v69
	v_pk_mul_f32 v[58:59], v[58:59], v[64:65]
	v_pk_mul_f32 v[56:57], v[62:63], v[56:57]
	v_pk_mul_f32 v[58:59], v[58:59], v[50:51]
	v_pk_mul_f32 v[50:51], v[60:61], v[68:69]
	s_nop 0
	v_pk_mul_f32 v[60:61], v[50:51], v[52:53]
	v_mul_f32_e32 v52, 0xbfb8aa3b, v46
	v_exp_f32_e32 v53, v52
	v_mul_f32_e32 v52, 0xbfb8aa3b, v47
	v_cvt_pk_bf16_f32 v50, v54, v55
	v_exp_f32_e32 v55, v52
	v_add_f32_e32 v53, 1.0, v53
	v_rcp_f32_e32 v54, v53
	v_cvt_pk_bf16_f32 v51, v56, v57
	v_add_f32_e32 v53, 1.0, v55
	v_cvt_pk_bf16_f32 v52, v58, v59
	v_rcp_f32_e32 v55, v53
	v_cvt_pk_bf16_f32 v53, v60, v61
	v_lshl_add_u64 v[56:57], v[66:67], 0, v[140:141]
	global_store_dwordx4 v[56:57], v[50:53], off
	v_pk_mul_f32 v[46:47], v[46:47], v[54:55]
	s_nop 0
	v_mul_f32_e32 v50, 0xbfb8aa3b, v48
	v_mul_f32_e32 v51, 0xbfb8aa3b, v49
	v_exp_f32_e32 v50, v50
	v_exp_f32_e32 v51, v51
	v_pk_mul_f32 v[38:39], v[46:47], v[38:39]
	v_add_f32_e32 v46, 1.0, v50
	v_add_f32_e32 v47, 1.0, v51
	v_mul_f32_e32 v50, 0xbfb8aa3b, v42
	v_mul_f32_e32 v51, 0xbfb8aa3b, v43
	v_rcp_f32_e32 v46, v46
	v_rcp_f32_e32 v47, v47
	v_exp_f32_e32 v50, v50
	v_exp_f32_e32 v51, v51
	v_pk_mul_f32 v[46:47], v[48:49], v[46:47]
	v_add_f32_e32 v48, 1.0, v50
	v_add_f32_e32 v49, 1.0, v51
	v_mul_f32_e32 v50, 0xbfb8aa3b, v44
	v_mul_f32_e32 v51, 0xbfb8aa3b, v45
	v_exp_f32_e32 v50, v50
; __device__ __forceinline__ float silu_fast(float v) { return v * __builtin_amdgcn_rcpf(1.f + __builtin_amdgcn_exp2f(-1.4426950408889634f * v)); }
; __device__ __forceinline__ u32x4 pack8(const f32x4 a, const f32x4 b) { u32x4 w; w.x = cvt_pk_bf16(a[0], a[1]); w.y = cvt_pk_bf16(a[2], a[3]); w.z = cvt_pk_bf16(b[0], b[1]); w.w = cvt_pk_bf16(b[2], b[3]); return w; }
; #define PG8_BAR __builtin_amdgcn_s_barrier()
;     __device__ __forceinline__ void operator()(const f32x4 (&acc)[2][2][4][2], const Unit& u, int wr, int wc, int fr, int fq) const {
;     ...
;             for (int m = 0; m < 4; ++m) { f32x4 h[2];
; #pragma unroll
;                 for (int n = 0; n < 2; ++n)
; #pragma unroll
;                     for (int j = 0; j < 4; ++j) h[n][j] = silu_fast(acc[ai][0][m][n][j]) * acc[ai][1][m][n][j];
;                 const int row = row0 + ai * HALF + m * 16;
;                 *(u32x4*)(base + ((size_t)(row >> 7) * (FF / 64) + (col0 >> 6)) * 8192 + (row & 127) * 64 + (col0 & 63)) = pack8(h[0], h[1]); }
;     ...
;         if (!has_next) break;
; #pragma unroll
;         for (int a = 0; a < 2; ++a)
; #pragma unroll
;             for (int b = 0; b < 2; ++b)
; #pragma unroll
;                 for (int m = 0; m < 4; ++m)
; #pragma unroll
;                     for (int n = 0; n < 2; ++n) acc[a][b][m][n] = (f32x4){0.f, 0.f, 0.f, 0.f};
;         cur = nxt; cA = nA; cB = nB; ++ui;
; #pragma unroll
;         for (int hh = 0; hh < 2; ++hh)
; #pragma unroll
;             for (int i = 0; i < 2; ++i) voffA[hh][i] = voffN[hh][i];
;         if (wr == 1) PG8_BAR;
	v_exp_f32_e32 v51, v51
	v_rcp_f32_e32 v48, v48
	v_rcp_f32_e32 v49, v49
	v_add_f32_e32 v50, 1.0, v50
	v_add_f32_e32 v51, 1.0, v51
	v_rcp_f32_e32 v50, v50
	v_rcp_f32_e32 v51, v51
	v_pk_mul_f32 v[42:43], v[42:43], v[48:49]
	v_pk_mul_f32 v[40:41], v[46:47], v[40:41]
	v_pk_mul_f32 v[42:43], v[42:43], v[34:35]
	v_pk_mul_f32 v[34:35], v[44:45], v[50:51]
	s_nop 0
	v_pk_mul_f32 v[44:45], v[34:35], v[36:37]
	v_mul_f32_e32 v35, 0xbfb8aa3b, v30
	v_exp_f32_e32 v36, v35
	v_mul_f32_e32 v35, 0xbfb8aa3b, v31
	v_exp_f32_e32 v37, v35
	v_cvt_pk_bf16_f32 v34, v38, v39
	v_add_f32_e32 v36, 1.0, v36
	v_rcp_f32_e32 v38, v36
	v_add_f32_e32 v36, 1.0, v37
	v_cvt_pk_bf16_f32 v35, v40, v41
	v_rcp_f32_e32 v39, v36
	v_cvt_pk_bf16_f32 v36, v42, v43
	v_cvt_pk_bf16_f32 v37, v44, v45
	global_store_dwordx4 v[56:57], v[34:37], off offset:2048
	v_pk_mul_f32 v[30:31], v[30:31], v[38:39]
	s_nop 0
	v_mul_f32_e32 v34, 0xbfb8aa3b, v32
	v_mul_f32_e32 v35, 0xbfb8aa3b, v33
	v_exp_f32_e32 v34, v34
	v_exp_f32_e32 v35, v35
	v_pk_mul_f32 v[22:23], v[30:31], v[22:23]
	v_add_f32_e32 v30, 1.0, v34
	v_add_f32_e32 v31, 1.0, v35
	v_mul_f32_e32 v34, 0xbfb8aa3b, v26
	v_mul_f32_e32 v35, 0xbfb8aa3b, v27
	v_rcp_f32_e32 v30, v30
	v_rcp_f32_e32 v31, v31
	v_exp_f32_e32 v34, v34
	v_exp_f32_e32 v35, v35
	v_pk_mul_f32 v[30:31], v[32:33], v[30:31]
	v_add_f32_e32 v32, 1.0, v34
	v_add_f32_e32 v33, 1.0, v35
	v_mul_f32_e32 v34, 0xbfb8aa3b, v28
	v_mul_f32_e32 v35, 0xbfb8aa3b, v29
	v_exp_f32_e32 v34, v34
	v_exp_f32_e32 v35, v35
	v_rcp_f32_e32 v32, v32
	v_rcp_f32_e32 v33, v33
	v_add_f32_e32 v34, 1.0, v34
	v_add_f32_e32 v35, 1.0, v35
	v_rcp_f32_e32 v34, v34
	v_rcp_f32_e32 v35, v35
	v_pk_mul_f32 v[26:27], v[26:27], v[32:33]
	v_pk_mul_f32 v[24:25], v[30:31], v[24:25]
	v_pk_mul_f32 v[26:27], v[26:27], v[18:19]
	v_pk_mul_f32 v[18:19], v[28:29], v[34:35]
	s_nop 0
	v_pk_mul_f32 v[28:29], v[18:19], v[20:21]
	v_mul_f32_e32 v20, 0xbfb8aa3b, v14
	v_exp_f32_e32 v21, v20
	v_mul_f32_e32 v20, 0xbfb8aa3b, v15
	v_cvt_pk_bf16_f32 v18, v22, v23
	v_exp_f32_e32 v23, v20
	v_add_f32_e32 v21, 1.0, v21
	v_rcp_f32_e32 v22, v21
	v_cvt_pk_bf16_f32 v19, v24, v25
	v_add_f32_e32 v21, 1.0, v23
	v_cvt_pk_bf16_f32 v20, v26, v27
	v_rcp_f32_e32 v23, v21
	v_cvt_pk_bf16_f32 v21, v28, v29
	v_lshl_add_u64 v[24:25], v[66:67], 0, v[142:143]
	global_store_dwordx4 v[24:25], v[18:21], off
	v_pk_mul_f32 v[14:15], v[14:15], v[22:23]
	s_nop 0
	v_mul_f32_e32 v18, 0xbfb8aa3b, v16
	v_mul_f32_e32 v19, 0xbfb8aa3b, v17
	v_exp_f32_e32 v18, v18
	v_exp_f32_e32 v19, v19
	v_pk_mul_f32 v[6:7], v[14:15], v[6:7]
	v_add_f32_e32 v14, 1.0, v18
	v_add_f32_e32 v15, 1.0, v19
	v_mul_f32_e32 v18, 0xbfb8aa3b, v10
	v_mul_f32_e32 v19, 0xbfb8aa3b, v11
	v_rcp_f32_e32 v14, v14
	v_rcp_f32_e32 v15, v15
	v_exp_f32_e32 v18, v18
	v_exp_f32_e32 v19, v19
	v_pk_mul_f32 v[14:15], v[16:17], v[14:15]
	v_add_f32_e32 v16, 1.0, v18
	v_add_f32_e32 v17, 1.0, v19
	v_mul_f32_e32 v18, 0xbfb8aa3b, v12
	v_mul_f32_e32 v19, 0xbfb8aa3b, v13
	v_exp_f32_e32 v18, v18
	v_exp_f32_e32 v19, v19
	v_rcp_f32_e32 v16, v16
	v_rcp_f32_e32 v17, v17
	v_add_f32_e32 v18, 1.0, v18
	v_add_f32_e32 v19, 1.0, v19
	v_rcp_f32_e32 v18, v18
	v_rcp_f32_e32 v19, v19
	v_pk_mul_f32 v[10:11], v[10:11], v[16:17]
	v_pk_mul_f32 v[8:9], v[14:15], v[8:9]
	v_pk_mul_f32 v[10:11], v[10:11], v[2:3]
	v_pk_mul_f32 v[2:3], v[12:13], v[18:19]
	s_nop 0
	v_pk_mul_f32 v[12:13], v[2:3], v[4:5]
	v_cvt_pk_bf16_f32 v2, v6, v7
	v_cvt_pk_bf16_f32 v3, v8, v9
	v_cvt_pk_bf16_f32 v4, v10, v11
	v_cvt_pk_bf16_f32 v5, v12, v13
	v_lshl_add_u64 v[6:7], v[66:67], 0, v[144:145]
	global_store_dwordx4 v[6:7], v[2:5], off
	s_cbranch_vccnz .LBB0_2331
	s_andn2_b64 vcc, exec, s[4:5]
	s_cbranch_vccnz .LBB0_2330
	s_branch .LBB0_2330
